# P6b pass U rewritten by hand too: lean int8 dot4 loop (token x rows staged through registers, butterfly lane reduction); pass V on the MFMA pipe as before
# speedup vs baseline: 1.0149x; 1.0149x over previous
; #define PU_SX() do { int a_ = 0, b_ = 0; _Pragma("unroll") for (int q_ = 0; q_ < 4; ++q_) { a_ = __builtin_amdgcn_sdot4((int)xq[0][q_], 0x01010101, a_, false); b_ = __builtin_amdgcn_sdot4((int)xq[1][q_], 0x01010101, b_, false); } sx15 = 240 * a_ - 16 * b_; } while (0)
; __device__ __forceinline__ void phase_peer_bucket(const Params& P, unsigned char* ws, int l, LAS unsigned char* lds, int bid, int G, int lane, int wave) {
;     ...
;             const unsigned char* X1Q = ws + WS_X1Q;
;             float xsc_v = 0.f; if (lane < 32) xsc_v = ((const float*)(ws + WS_XSC))[nbase + lane];
;             int tcur = peer3_next_nonempty(gstv, 0); int tnx = peer3_next_nonempty(gstv, tcur + 1); int tend = __builtin_amdgcn_readlane(gstv, tcur + 1);
;             u4 xq[2];
;             { const unsigned char* p = X1Q + (size_t)(nbase + tcur) * 2048u + (unsigned)lane * 16u; xq[0] = __builtin_nontemporal_load((const u4*)p); xq[1] = __builtin_nontemporal_load((const u4*)(p + 1024)); }
;             int lt = tnx, lts = (lt < 32) ? __builtin_amdgcn_readlane(gstv, lt) : 0x7fffffff;
;             float xs = __int_as_float(__builtin_amdgcn_readlane(__float_as_int(xsc_v), tcur));
;             int evn = 0; float wvn = 0.f;
;             if (lane < total) { evn = __builtin_nontemporal_load(FE + lane); wvn = __builtin_nontemporal_load(FW + lane); }
;     ...
;             int sx15; PU_SX();
.Lq_entry:
	s_mul_i32 s100, s29, 0x4400
	s_mov_b32 s65, 0x1010101
	s_mov_b32 s22, 0xf000f
	s_mov_b32 s23, 0xf000f
	v_and_b32_e32 v117, 1, v208
	v_cmp_eq_u32_e64 s[38:39], 1, v117
	v_and_b32_e32 v117, 2, v208
	v_cmp_eq_u32_e64 s[42:43], 2, v117
	s_add_u32 s52, s12, s14
	s_addc_u32 s53, s13, s15
	s_add_u32 s52, s52, 0xa000000
	s_addc_u32 s53, s53, 0
	s_sub_u32 s58, s16, 0x8000000
	s_subb_u32 s59, s17, 0
	v_readlane_b32 s4, v254, 52
	s_lshl_b32 s4, s4, 16
	s_add_u32 s18, s12, 0x4e000000
	s_addc_u32 s19, s13, 0
	s_add_u32 s18, s18, s4
	s_addc_u32 s19, s19, 0
	s_lshl_b32 s4, s8, 11
	s_add_u32 s26, s12, 0x6b000000
	s_addc_u32 s27, s13, 0
	s_add_u32 s26, s26, s4
	s_addc_u32 s27, s27, 0
	s_add_u32 s6, s12, 0x6c000000
	s_addc_u32 s7, s13, 0
	v_mov_b32_e32 v201, 0
	v_add_lshl_u32 v117, v208, s8, 2
	v_cmp_gt_u32_e32 vcc, 32, v208
	s_and_saveexec_b64 s[4:5], vcc
	global_load_dword v201, v117, s[6:7]
	s_or_b64 exec, exec, s[4:5]
	v_mov_b32_e32 v233, 0
	v_mov_b32_e32 v83, 0
	v_mov_b32_e32 v87, 0
	v_mov_b32_e32 v84, 0
	v_mov_b32_e32 v88, 0
	v_mov_b32_e32 v85, 0
	v_mov_b32_e32 v89, 0
	v_mov_b32_e32 v86, 0
	v_mov_b32_e32 v90, 0
	v_mov_b32_e32 v74, 0
	v_mov_b32_e32 v78, 0
	v_add_u32_e32 v118, 0x4000000, v212
	s_and_saveexec_b64 s[4:5], s[40:41]
	global_load_dword v74, v212, s[58:59] nt
	global_load_dword v78, v118, s[58:59] nt
	s_or_b64 exec, exec, s[4:5]
	s_mov_b32 s31, 0
.Lq_nn1:
	s_cmp_gt_u32 s31, 31
	s_cbranch_scc1 .Lq_nnd1
	s_add_u32 s4, s31, 1
	v_readlane_b32 s5, v81, s4
	v_readlane_b32 s6, v81, s31
	s_cmp_lg_u32 s5, s6
	s_cbranch_scc1 .Lq_nnd1
	s_add_u32 s31, s31, 1
	s_branch .Lq_nn1
.Lq_nnd1:
	s_mov_b32 s35, 0
	s_mov_b32 s50, s31
	s_mov_b32 s56, 0
	s_mov_b32 s9, 0
	s_mov_b32 s34, 0
	s_mov_b32 s11, 0
	s_mov_b32 s62, 0
.Lq_stp:
	s_cmp_gt_u32 s50, 31
	s_cbranch_scc1 .Lq_stpw
	v_readlane_b32 s4, v81, s50
	s_cmp_lt_u32 s4, 20
	s_cbranch_scc0 .Lq_stpw
	s_and_b32 s4, s56, 7
	s_mul_i32 s4, s4, 0x810
	s_add_u32 s44, s100, s4
	s_lshl_b32 s5, s50, 11
	s_add_u32 s6, s26, s5
	s_addc_u32 s7, s27, 0
	s_add_u32 s56, s56, 1
	global_load_dwordx4 v[128:131], v206, s[6:7] nt
	global_load_dwordx4 v[132:135], v206, s[6:7] offset:1024 nt
	s_bitset1_b32 s62, 0
	s_add_u32 s50, s50, 1

; #define PU_SX() do { int a_ = 0, b_ = 0; _Pragma("unroll") for (int q_ = 0; q_ < 4; ++q_) { a_ = __builtin_amdgcn_sdot4((int)xq[0][q_], 0x01010101, a_, false); b_ = __builtin_amdgcn_sdot4((int)xq[1][q_], 0x01010101, b_, false); } sx15 = 240 * a_ - 16 * b_; } while (0)
; __device__ __forceinline__ void phase_peer_bucket(const Params& P, unsigned char* ws, int l, LAS unsigned char* lds, int bid, int G, int lane, int wave) {
;     ...
;             { const unsigned char* p = X1Q + (size_t)(nbase + tcur) * 2048u + (unsigned)lane * 16u; xq[0] = __builtin_nontemporal_load((const u4*)p); xq[1] = __builtin_nontemporal_load((const u4*)(p + 1024)); }
;             int lt = tnx, lts = (lt < 32) ? __builtin_amdgcn_readlane(gstv, lt) : 0x7fffffff;
;             float xs = __int_as_float(__builtin_amdgcn_readlane(__float_as_int(xsc_v), tcur));
;             int evn = 0; float wvn = 0.f;
;             if (lane < total) { evn = __builtin_nontemporal_load(FE + lane); wvn = __builtin_nontemporal_load(FW + lane); }
;     ...
;             int sx15; PU_SX();
.Lq_nnd2:
	s_cmp_gt_u32 s50, 31
	s_cbranch_scc1 .Lq_stpw
	v_readlane_b32 s4, v81, s50
	s_cmp_lt_u32 s4, 20
	s_cbranch_scc0 .Lq_stpw
	s_and_b32 s4, s56, 7
	s_mul_i32 s4, s4, 0x810
	s_add_u32 s45, s100, s4
	s_lshl_b32 s5, s50, 11
	s_add_u32 s6, s26, s5
	s_addc_u32 s7, s27, 0
	s_add_u32 s56, s56, 1
	global_load_dwordx4 v[136:139], v206, s[6:7] nt
	global_load_dwordx4 v[140:143], v206, s[6:7] offset:1024 nt
	s_bitset1_b32 s62, 1
	s_add_u32 s50, s50, 1

; #define PU_SX() do { int a_ = 0, b_ = 0; _Pragma("unroll") for (int q_ = 0; q_ < 4; ++q_) { a_ = __builtin_amdgcn_sdot4((int)xq[0][q_], 0x01010101, a_, false); b_ = __builtin_amdgcn_sdot4((int)xq[1][q_], 0x01010101, b_, false); } sx15 = 240 * a_ - 16 * b_; } while (0)
; __device__ __forceinline__ void phase_peer_bucket(const Params& P, unsigned char* ws, int l, LAS unsigned char* lds, int bid, int G, int lane, int wave) {
;     ...
;             { const unsigned char* p = X1Q + (size_t)(nbase + tcur) * 2048u + (unsigned)lane * 16u; xq[0] = __builtin_nontemporal_load((const u4*)p); xq[1] = __builtin_nontemporal_load((const u4*)(p + 1024)); }
;             int lt = tnx, lts = (lt < 32) ? __builtin_amdgcn_readlane(gstv, lt) : 0x7fffffff;
;             float xs = __int_as_float(__builtin_amdgcn_readlane(__float_as_int(xsc_v), tcur));
;             int evn = 0; float wvn = 0.f;
;             if (lane < total) { evn = __builtin_nontemporal_load(FE + lane); wvn = __builtin_nontemporal_load(FW + lane); }
;     ...
;             int sx15; PU_SX();
.Lq_nnd3:
	s_cmp_gt_u32 s50, 31
	s_cbranch_scc1 .Lq_stpw
	v_readlane_b32 s4, v81, s50
	s_cmp_lt_u32 s4, 20
	s_cbranch_scc0 .Lq_stpw
	s_and_b32 s4, s56, 7
	s_mul_i32 s4, s4, 0x810
	s_add_u32 s46, s100, s4
	s_lshl_b32 s5, s50, 11
	s_add_u32 s6, s26, s5
	s_addc_u32 s7, s27, 0
	s_add_u32 s56, s56, 1
	global_load_dwordx4 v[144:147], v206, s[6:7] nt
	global_load_dwordx4 v[148:151], v206, s[6:7] offset:1024 nt
	s_bitset1_b32 s62, 2
	s_add_u32 s50, s50, 1

; #define PU_SX() do { int a_ = 0, b_ = 0; _Pragma("unroll") for (int q_ = 0; q_ < 4; ++q_) { a_ = __builtin_amdgcn_sdot4((int)xq[0][q_], 0x01010101, a_, false); b_ = __builtin_amdgcn_sdot4((int)xq[1][q_], 0x01010101, b_, false); } sx15 = 240 * a_ - 16 * b_; } while (0)
; __device__ __forceinline__ void phase_peer_bucket(const Params& P, unsigned char* ws, int l, LAS unsigned char* lds, int bid, int G, int lane, int wave) {
;     ...
;             { const unsigned char* p = X1Q + (size_t)(nbase + tcur) * 2048u + (unsigned)lane * 16u; xq[0] = __builtin_nontemporal_load((const u4*)p); xq[1] = __builtin_nontemporal_load((const u4*)(p + 1024)); }
;             int lt = tnx, lts = (lt < 32) ? __builtin_amdgcn_readlane(gstv, lt) : 0x7fffffff;
;             float xs = __int_as_float(__builtin_amdgcn_readlane(__float_as_int(xsc_v), tcur));
;             int evn = 0; float wvn = 0.f;
;             if (lane < total) { evn = __builtin_nontemporal_load(FE + lane); wvn = __builtin_nontemporal_load(FW + lane); }
;     ...
;             int sx15; PU_SX();
.Lq_nnd4:
	s_cmp_gt_u32 s50, 31
	s_cbranch_scc1 .Lq_stpw
	v_readlane_b32 s4, v81, s50
	s_cmp_lt_u32 s4, 20
	s_cbranch_scc0 .Lq_stpw
	s_and_b32 s4, s56, 7
	s_mul_i32 s4, s4, 0x810
	s_add_u32 s47, s100, s4
	s_lshl_b32 s5, s50, 11
	s_add_u32 s6, s26, s5
	s_addc_u32 s7, s27, 0
	s_add_u32 s56, s56, 1
	global_load_dwordx4 v[152:155], v206, s[6:7] nt
	global_load_dwordx4 v[156:159], v206, s[6:7] offset:1024 nt
	s_bitset1_b32 s62, 3
	s_add_u32 s50, s50, 1

; __device__ __forceinline__ void phase_peer_bucket(const Params& P, unsigned char* ws, int l, LAS unsigned char* lds, int bid, int G, int lane, int wave) {
;     ...
;             for (int blk = 0; blk < total; blk += 64) { const int blen = (total - blk) < 64 ? (total - blk) : 64, ng = blen / PG;
;                 const int ev = evn; const float wv = wvn;
;                 if (blk + 64 + lane < total) { evn = __builtin_nontemporal_load(FE + blk + 64 + lane); wvn = __builtin_nontemporal_load(FW + blk + 64 + lane); }
;                 const float us = USC[ev], vs = VSC[ev];
;                 float xsv = 0.f;
;                 if (ng == 16) {
;                     const bool nextfull = blk + 128 <= total;
;                     if (!pre) { PU_ROWS(A, 0); PU_ROWS(B, 1); PU_ROWS(C, 2); }
.Lq_nnd5:
.Lq_stpw:
	s_waitcnt vmcnt(0)
	s_bitcmp1_b32 s62, 0
	s_cbranch_scc0 .Lq_stps6
	v_add_u32_e32 v117, s44, v206
	s_bitset0_b32 s62, 0
	ds_write_b128 v117, v[128:131]
	ds_write_b128 v117, v[132:135] offset:1024
.Lq_stps6:
	s_bitcmp1_b32 s62, 1
	s_cbranch_scc0 .Lq_stps7
	v_add_u32_e32 v117, s45, v206
	s_bitset0_b32 s62, 1
	ds_write_b128 v117, v[136:139]
	ds_write_b128 v117, v[140:143] offset:1024
.Lq_stps7:
	s_bitcmp1_b32 s62, 2
	s_cbranch_scc0 .Lq_stps8
	v_add_u32_e32 v117, s46, v206
	s_bitset0_b32 s62, 2
	ds_write_b128 v117, v[144:147]
	ds_write_b128 v117, v[148:151] offset:1024
.Lq_stps8:
	s_bitcmp1_b32 s62, 3
	s_cbranch_scc0 .Lq_stps9
	v_add_u32_e32 v117, s47, v206
	s_bitset0_b32 s62, 3
	ds_write_b128 v117, v[152:155]
	ds_write_b128 v117, v[156:159] offset:1024
.Lq_stps9:
	s_cmp_gt_u32 s50, 31
	s_cbranch_scc1 .Lq_stpd
	v_readlane_b32 s4, v81, s50
	s_cmp_lt_u32 s4, 20
	s_cbranch_scc1 .Lq_stp
.Lq_stpd:
	s_waitcnt vmcnt(0)
	v_mov_b32_e32 v73, v74
	v_lshlrev_b32_e32 v75, 10, v74
	v_mov_b32_e32 v77, v78
	v_lshlrev_b32_e32 v117, 2, v74
	v_add_u32_e32 v118, 0x40000, v117
	global_load_dword v79, v117, s[18:19]
	global_load_dword v82, v118, s[18:19]
	v_mov_b32_e32 v74, 0
	v_mov_b32_e32 v78, 0
	s_add_u32 s4, s34, 64
	v_add_u32_e32 v119, s4, v208
	v_cmp_gt_u32_e32 vcc, s28, v119
	v_lshlrev_b32_e32 v119, 2, v119
	v_add_u32_e32 v120, 0x4000000, v119
	s_and_saveexec_b64 s[6:7], vcc
	global_load_dword v74, v119, s[58:59] nt
	global_load_dword v78, v120, s[58:59] nt
	s_or_b64 exec, exec, s[6:7]
	v_readlane_b32 s36, v75, 0
	v_readlane_b32 s5, v75, 1
	v_readlane_b32 s6, v75, 2
	v_readlane_b32 s7, v75, 3
	v_add_u32_e32 v113, s36, v206
	v_add_u32_e32 v114, s5, v206
	v_add_u32_e32 v115, s6, v206
	v_add_u32_e32 v116, s7, v206
	global_load_dwordx4 v[0:3], v113, s[52:53]
	global_load_dwordx4 v[4:7], v114, s[52:53]
	global_load_dwordx4 v[8:11], v115, s[52:53]
	global_load_dwordx4 v[12:15], v116, s[52:53]
	v_readlane_b32 s36, v75, 4
	v_readlane_b32 s5, v75, 5
	v_readlane_b32 s6, v75, 6
	v_readlane_b32 s7, v75, 7
	v_add_u32_e32 v113, s36, v206
	v_add_u32_e32 v114, s5, v206
	v_add_u32_e32 v115, s6, v206
	v_add_u32_e32 v116, s7, v206
	global_load_dwordx4 v[16:19], v113, s[52:53]
	global_load_dwordx4 v[20:23], v114, s[52:53]
	global_load_dwordx4 v[24:27], v115, s[52:53]
	global_load_dwordx4 v[28:31], v116, s[52:53]
	v_readlane_b32 s36, v75, 8
	v_readlane_b32 s5, v75, 9
	v_readlane_b32 s6, v75, 10
	v_readlane_b32 s7, v75, 11
	v_add_u32_e32 v113, s36, v206
	v_add_u32_e32 v114, s5, v206
	v_add_u32_e32 v115, s6, v206
	v_add_u32_e32 v116, s7, v206
	global_load_dwordx4 v[32:35], v113, s[52:53]
	global_load_dwordx4 v[36:39], v114, s[52:53]
	global_load_dwordx4 v[40:43], v115, s[52:53]
	global_load_dwordx4 v[44:47], v116, s[52:53]
	s_branch .Lq_g0
.Lq_block:
	v_mov_b32_e32 v73, v74
	v_lshlrev_b32_e32 v75, 10, v74
	v_mov_b32_e32 v77, v78
	v_lshlrev_b32_e32 v117, 2, v74
	v_add_u32_e32 v118, 0x40000, v117
	global_load_dword v79, v117, s[18:19]
	global_load_dword v82, v118, s[18:19]
	v_mov_b32_e32 v74, 0
	v_mov_b32_e32 v78, 0
	s_add_u32 s4, s34, 64
	v_add_u32_e32 v119, s4, v208
	v_cmp_gt_u32_e32 vcc, s28, v119
	v_lshlrev_b32_e32 v119, 2, v119
	v_add_u32_e32 v120, 0x4000000, v119
	s_and_saveexec_b64 s[6:7], vcc
	global_load_dword v74, v119, s[58:59] nt
	global_load_dword v78, v120, s[58:59] nt
	s_or_b64 exec, exec, s[6:7]
.Lq_g0:
	s_add_u32 s11, s34, 0
	s_cmp_gt_u32 s50, 31
	s_cbranch_scc1 .Lq_stdg0
	s_add_u32 s36, s11, 20
	v_readlane_b32 s4, v81, s50
	s_cmp_lt_u32 s4, s36
	s_cbranch_scc1 .Lq_stxg0
.Lq_stdg0:
	s_cmp_ge_u32 s11, s35
	s_cbranch_scc1 .Lq_sw0
.Lq_swret0:
	s_waitcnt vmcnt(8)
	s_bitcmp1_b32 s62, 1
	s_cbranch_scc1 .Lq_fin0
; #define LAS __attribute__((address_space(3)))
; __device__ __forceinline__ int wave_isum4_t(const int (&d)[4], int lane) {
;     const bool o1 = lane & 1, o2 = lane & 2;
;     int a = o1 ? d[1] : d[0], b = o1 ? d[0] : d[1], c = o1 ? d[3] : d[2], e = o1 ? d[2] : d[3];
;     a += __builtin_amdgcn_update_dpp(0, b, 0xB1, 0xf, 0xf, true);
;     c += __builtin_amdgcn_update_dpp(0, e, 0xB1, 0xf, 0xf, true);
;     int f = o2 ? c : a, g = o2 ? a : c;
;     f += __builtin_amdgcn_update_dpp(0, g, 0x4E, 0xf, 0xf, true);
;     f += __builtin_amdgcn_update_dpp(0, f, 0x124, 0xf, 0xf, true);
;     f += __builtin_amdgcn_update_dpp(0, f, 0x128, 0xf, 0xf, true);
; __device__ __forceinline__ void peer3_dots(const u4 (&R)[PG][2], const u4 (&xq)[2], int sx15, LAS int* redrow, int g) {
;     ...
;     for (int k = 0; k < 4; ++k) { int a = 0, ah = 0;
; #pragma unroll
;         for (int q = 0; q < 4; ++q) { const unsigned w = R[k][0][q];
;             a = __builtin_amdgcn_sdot4((int)(w & 0x0f0f0f0fu), (int)xq[0][q], a, false); ah = __builtin_amdgcn_sdot4((int)(w & 0xf0f0f0f0u), (int)xq[1][q], ah, false); }
;         d[k] = 32 * a + 2 * ah - sx15; }
;     u4 w; w.x = (unsigned)d[0]; w.y = (unsigned)d[1]; w.z = (unsigned)d[2]; w.w = (unsigned)d[3];
;     *(LAS u4*)(redrow + 4 * g) = w;
.Lq_finret0:
	v_and_b32_e32 v95, 0xf0f0f0f, v0
	v_and_b32_e32 v99, 0xf0f0f0f0, v0
	v_and_b32_e32 v96, 0xf0f0f0f, v1
	v_and_b32_e32 v100, 0xf0f0f0f0, v1
	v_dot4_i32_i8 v103, v95, v64, 0
	v_dot4_i32_i8 v104, v99, v68, 0
	v_and_b32_e32 v97, 0xf0f0f0f, v2
	v_and_b32_e32 v101, 0xf0f0f0f0, v2
	v_dot4_i32_i8 v103, v96, v65, v103
	v_dot4_i32_i8 v104, v100, v69, v104
	v_and_b32_e32 v98, 0xf0f0f0f, v3
	v_and_b32_e32 v102, 0xf0f0f0f0, v3
	v_dot4_i32_i8 v103, v97, v66, v103
	v_dot4_i32_i8 v104, v101, v70, v104
	v_dot4_i32_i8 v103, v98, v67, v103
	v_dot4_i32_i8 v104, v102, v71, v104
	v_and_b32_e32 v95, 0xf0f0f0f, v4
	v_and_b32_e32 v99, 0xf0f0f0f0, v4
	v_and_b32_e32 v96, 0xf0f0f0f, v5
	v_and_b32_e32 v100, 0xf0f0f0f0, v5
	v_lshl_add_u32 v105, v103, 4, v104
	v_lshl_add_u32 v91, v105, 1, v72
	v_dot4_i32_i8 v126, v95, v64, 0
	v_dot4_i32_i8 v127, v99, v68, 0
	v_and_b32_e32 v97, 0xf0f0f0f, v6
	v_and_b32_e32 v101, 0xf0f0f0f0, v6
	v_dot4_i32_i8 v126, v96, v65, v126
	v_dot4_i32_i8 v127, v100, v69, v127
	v_and_b32_e32 v98, 0xf0f0f0f, v7
	v_and_b32_e32 v102, 0xf0f0f0f0, v7
	v_dot4_i32_i8 v126, v97, v66, v126
	v_dot4_i32_i8 v127, v101, v70, v127
	v_dot4_i32_i8 v126, v98, v67, v126
	v_dot4_i32_i8 v127, v102, v71, v127
	v_and_b32_e32 v95, 0xf0f0f0f, v8
	v_and_b32_e32 v99, 0xf0f0f0f0, v8
	v_and_b32_e32 v96, 0xf0f0f0f, v9
	v_and_b32_e32 v100, 0xf0f0f0f0, v9
	v_lshl_add_u32 v105, v126, 4, v127
	v_lshl_add_u32 v92, v105, 1, v72
	v_dot4_i32_i8 v103, v95, v64, 0
	v_dot4_i32_i8 v104, v99, v68, 0
	v_and_b32_e32 v97, 0xf0f0f0f, v10
	v_and_b32_e32 v101, 0xf0f0f0f0, v10
	v_dot4_i32_i8 v103, v96, v65, v103
	v_dot4_i32_i8 v104, v100, v69, v104
	v_and_b32_e32 v98, 0xf0f0f0f, v11
	v_and_b32_e32 v102, 0xf0f0f0f0, v11
	v_dot4_i32_i8 v103, v97, v66, v103
	v_dot4_i32_i8 v104, v101, v70, v104
	v_dot4_i32_i8 v103, v98, v67, v103
	v_dot4_i32_i8 v104, v102, v71, v104
	v_and_b32_e32 v95, 0xf0f0f0f, v12
	v_and_b32_e32 v99, 0xf0f0f0f0, v12
	v_and_b32_e32 v96, 0xf0f0f0f, v13
	v_and_b32_e32 v100, 0xf0f0f0f0, v13
	v_lshl_add_u32 v105, v103, 4, v104
	v_lshl_add_u32 v93, v105, 1, v72
	v_dot4_i32_i8 v126, v95, v64, 0
	v_dot4_i32_i8 v127, v99, v68, 0
	v_and_b32_e32 v97, 0xf0f0f0f, v14
	v_and_b32_e32 v101, 0xf0f0f0f0, v14
	v_dot4_i32_i8 v126, v96, v65, v126
	v_dot4_i32_i8 v127, v100, v69, v127
	v_and_b32_e32 v98, 0xf0f0f0f, v15
	v_and_b32_e32 v102, 0xf0f0f0f0, v15
	v_dot4_i32_i8 v126, v97, v66, v126
	v_dot4_i32_i8 v127, v101, v70, v127
	v_dot4_i32_i8 v126, v98, v67, v126
	v_dot4_i32_i8 v127, v102, v71, v127
	v_readlane_b32 s36, v75, 12
	v_readlane_b32 s5, v75, 13
	v_readlane_b32 s6, v75, 14
	v_lshl_add_u32 v105, v126, 4, v127
	v_lshl_add_u32 v94, v105, 1, v72
	v_cndmask_b32_e64 v107, v92, v91, s[38:39]
	v_cndmask_b32_e64 v109, v94, v93, s[38:39]
	v_cndmask_b32_e64 v106, v91, v92, s[38:39]
	v_cndmask_b32_e64 v108, v93, v94, s[38:39]
	v_add_u32_dpp v106, v107, v106 quad_perm:[1,0,3,2] row_mask:0xf bank_mask:0xf
	v_add_u32_dpp v108, v109, v108 quad_perm:[1,0,3,2] row_mask:0xf bank_mask:0xf
	v_readlane_b32 s7, v75, 15
	v_cndmask_b32_e64 v111, v108, v106, s[42:43]
	v_cndmask_b32_e64 v110, v106, v108, s[42:43]
	v_add_u32_e32 v113, s36, v206
	v_add_u32_e32 v114, s5, v206
	v_add_u32_dpp v110, v111, v110 quad_perm:[2,3,0,1] row_mask:0xf bank_mask:0xf
	v_add_u32_e32 v115, s6, v206
	v_add_u32_e32 v116, s7, v206
	v_add_u32_dpp v110, v110, v110 row_ror:4 row_mask:0xf bank_mask:0xf
	global_load_dwordx4 v[48:51], v113, s[52:53]
	global_load_dwordx4 v[52:55], v114, s[52:53]
	v_add_u32_dpp v110, v110, v110 row_ror:8 row_mask:0xf bank_mask:0xf
	global_load_dwordx4 v[56:59], v115, s[52:53]
	global_load_dwordx4 v[60:63], v116, s[52:53]
	s_mov_b64 exec, s[22:23]
	v_mov_b32_e32 v83, v110
	v_mov_b32_e32 v87, s10
	s_mov_b64 exec, -1
.Lq_g1:
	s_add_u32 s11, s34, 4
	s_cmp_ge_u32 s11, s28
	s_cbranch_scc1 .Lq_end
	s_cmp_gt_u32 s50, 31
	s_cbranch_scc1 .Lq_stdg1
	s_add_u32 s36, s11, 20
	v_readlane_b32 s4, v81, s50
	s_cmp_lt_u32 s4, s36
	s_cbranch_scc1 .Lq_stxg1

; #define LAS __attribute__((address_space(3)))
; __device__ __forceinline__ int wave_isum4_t(const int (&d)[4], int lane) {
;     const bool o1 = lane & 1, o2 = lane & 2;
;     int a = o1 ? d[1] : d[0], b = o1 ? d[0] : d[1], c = o1 ? d[3] : d[2], e = o1 ? d[2] : d[3];
;     a += __builtin_amdgcn_update_dpp(0, b, 0xB1, 0xf, 0xf, true);
;     c += __builtin_amdgcn_update_dpp(0, e, 0xB1, 0xf, 0xf, true);
;     int f = o2 ? c : a, g = o2 ? a : c;
;     f += __builtin_amdgcn_update_dpp(0, g, 0x4E, 0xf, 0xf, true);
;     f += __builtin_amdgcn_update_dpp(0, f, 0x124, 0xf, 0xf, true);
;     f += __builtin_amdgcn_update_dpp(0, f, 0x128, 0xf, 0xf, true);
; __device__ __forceinline__ void peer3_dots(const u4 (&R)[PG][2], const u4 (&xq)[2], int sx15, LAS int* redrow, int g) {
;     ...
;     for (int k = 0; k < 4; ++k) { int a = 0, ah = 0;
; #pragma unroll
;         for (int q = 0; q < 4; ++q) { const unsigned w = R[k][0][q];
;             a = __builtin_amdgcn_sdot4((int)(w & 0x0f0f0f0fu), (int)xq[0][q], a, false); ah = __builtin_amdgcn_sdot4((int)(w & 0xf0f0f0f0u), (int)xq[1][q], ah, false); }
;         d[k] = 32 * a + 2 * ah - sx15; }
;     u4 w; w.x = (unsigned)d[0]; w.y = (unsigned)d[1]; w.z = (unsigned)d[2]; w.w = (unsigned)d[3];
;     *(LAS u4*)(redrow + 4 * g) = w;
.Lq_swret1:
	s_waitcnt vmcnt(8)
	s_bitcmp1_b32 s62, 2
	s_cbranch_scc1 .Lq_fin1
.Lq_finret1:
	v_and_b32_e32 v95, 0xf0f0f0f, v16
	v_and_b32_e32 v99, 0xf0f0f0f0, v16
	v_and_b32_e32 v96, 0xf0f0f0f, v17
	v_and_b32_e32 v100, 0xf0f0f0f0, v17
	v_dot4_i32_i8 v103, v95, v64, 0
	v_dot4_i32_i8 v104, v99, v68, 0
	v_and_b32_e32 v97, 0xf0f0f0f, v18
	v_and_b32_e32 v101, 0xf0f0f0f0, v18
	v_dot4_i32_i8 v103, v96, v65, v103
	v_dot4_i32_i8 v104, v100, v69, v104
	v_and_b32_e32 v98, 0xf0f0f0f, v19
	v_and_b32_e32 v102, 0xf0f0f0f0, v19
	v_dot4_i32_i8 v103, v97, v66, v103
	v_dot4_i32_i8 v104, v101, v70, v104
	v_dot4_i32_i8 v103, v98, v67, v103
	v_dot4_i32_i8 v104, v102, v71, v104
	v_and_b32_e32 v95, 0xf0f0f0f, v20
	v_and_b32_e32 v99, 0xf0f0f0f0, v20
	v_and_b32_e32 v96, 0xf0f0f0f, v21
	v_and_b32_e32 v100, 0xf0f0f0f0, v21
	v_lshl_add_u32 v105, v103, 4, v104
	v_lshl_add_u32 v91, v105, 1, v72
	v_dot4_i32_i8 v126, v95, v64, 0
	v_dot4_i32_i8 v127, v99, v68, 0
	v_and_b32_e32 v97, 0xf0f0f0f, v22
	v_and_b32_e32 v101, 0xf0f0f0f0, v22
	v_dot4_i32_i8 v126, v96, v65, v126
	v_dot4_i32_i8 v127, v100, v69, v127
	v_and_b32_e32 v98, 0xf0f0f0f, v23
	v_and_b32_e32 v102, 0xf0f0f0f0, v23
	v_dot4_i32_i8 v126, v97, v66, v126
	v_dot4_i32_i8 v127, v101, v70, v127
	v_dot4_i32_i8 v126, v98, v67, v126
	v_dot4_i32_i8 v127, v102, v71, v127
	v_and_b32_e32 v95, 0xf0f0f0f, v24
	v_and_b32_e32 v99, 0xf0f0f0f0, v24
	v_and_b32_e32 v96, 0xf0f0f0f, v25
	v_and_b32_e32 v100, 0xf0f0f0f0, v25
	v_lshl_add_u32 v105, v126, 4, v127
	v_lshl_add_u32 v92, v105, 1, v72
	v_dot4_i32_i8 v103, v95, v64, 0
	v_dot4_i32_i8 v104, v99, v68, 0
	v_and_b32_e32 v97, 0xf0f0f0f, v26
	v_and_b32_e32 v101, 0xf0f0f0f0, v26
	v_dot4_i32_i8 v103, v96, v65, v103
	v_dot4_i32_i8 v104, v100, v69, v104
	v_and_b32_e32 v98, 0xf0f0f0f, v27
	v_and_b32_e32 v102, 0xf0f0f0f0, v27
	v_dot4_i32_i8 v103, v97, v66, v103
	v_dot4_i32_i8 v104, v101, v70, v104
	v_dot4_i32_i8 v103, v98, v67, v103
	v_dot4_i32_i8 v104, v102, v71, v104
	v_and_b32_e32 v95, 0xf0f0f0f, v28
	v_and_b32_e32 v99, 0xf0f0f0f0, v28
	v_and_b32_e32 v96, 0xf0f0f0f, v29
	v_and_b32_e32 v100, 0xf0f0f0f0, v29
	v_lshl_add_u32 v105, v103, 4, v104
	v_lshl_add_u32 v93, v105, 1, v72
	v_dot4_i32_i8 v126, v95, v64, 0
	v_dot4_i32_i8 v127, v99, v68, 0
	v_and_b32_e32 v97, 0xf0f0f0f, v30
	v_and_b32_e32 v101, 0xf0f0f0f0, v30
	v_dot4_i32_i8 v126, v96, v65, v126
	v_dot4_i32_i8 v127, v100, v69, v127
	v_and_b32_e32 v98, 0xf0f0f0f, v31
	v_and_b32_e32 v102, 0xf0f0f0f0, v31
	v_dot4_i32_i8 v126, v97, v66, v126
	v_dot4_i32_i8 v127, v101, v70, v127
	v_dot4_i32_i8 v126, v98, v67, v126
	v_dot4_i32_i8 v127, v102, v71, v127
	v_readlane_b32 s36, v75, 16
	v_readlane_b32 s5, v75, 17
	v_readlane_b32 s6, v75, 18
	v_lshl_add_u32 v105, v126, 4, v127
	v_lshl_add_u32 v94, v105, 1, v72
	v_cndmask_b32_e64 v107, v92, v91, s[38:39]
	v_cndmask_b32_e64 v109, v94, v93, s[38:39]
	v_cndmask_b32_e64 v106, v91, v92, s[38:39]
	v_cndmask_b32_e64 v108, v93, v94, s[38:39]
	v_add_u32_dpp v106, v107, v106 quad_perm:[1,0,3,2] row_mask:0xf bank_mask:0xf
	v_add_u32_dpp v108, v109, v108 quad_perm:[1,0,3,2] row_mask:0xf bank_mask:0xf
	v_readlane_b32 s7, v75, 19
	v_cndmask_b32_e64 v111, v108, v106, s[42:43]
	v_cndmask_b32_e64 v110, v106, v108, s[42:43]
	v_add_u32_e32 v113, s36, v206
	v_add_u32_e32 v114, s5, v206
	v_add_u32_dpp v110, v111, v110 quad_perm:[2,3,0,1] row_mask:0xf bank_mask:0xf
	v_add_u32_e32 v115, s6, v206
	v_add_u32_e32 v116, s7, v206
	v_add_u32_dpp v110, v110, v110 row_ror:4 row_mask:0xf bank_mask:0xf
	global_load_dwordx4 v[0:3], v113, s[52:53]
	global_load_dwordx4 v[4:7], v114, s[52:53]
	v_add_u32_dpp v110, v110, v110 row_ror:8 row_mask:0xf bank_mask:0xf
	global_load_dwordx4 v[8:11], v115, s[52:53]
	global_load_dwordx4 v[12:15], v116, s[52:53]
	s_lshl_b64 exec, s[22:23], 4
	v_mov_b32_e32 v83, v110
	v_mov_b32_e32 v87, s10
	s_mov_b64 exec, -1
.Lq_g2:
	s_add_u32 s11, s34, 8
	s_cmp_ge_u32 s11, s28
	s_cbranch_scc1 .Lq_end
	s_cmp_gt_u32 s50, 31
	s_cbranch_scc1 .Lq_stdg2
	s_add_u32 s36, s11, 20
	v_readlane_b32 s4, v81, s50
	s_cmp_lt_u32 s4, s36
	s_cbranch_scc1 .Lq_stxg2

; #define LAS __attribute__((address_space(3)))
; __device__ __forceinline__ int wave_isum4_t(const int (&d)[4], int lane) {
;     const bool o1 = lane & 1, o2 = lane & 2;
;     int a = o1 ? d[1] : d[0], b = o1 ? d[0] : d[1], c = o1 ? d[3] : d[2], e = o1 ? d[2] : d[3];
;     a += __builtin_amdgcn_update_dpp(0, b, 0xB1, 0xf, 0xf, true);
;     c += __builtin_amdgcn_update_dpp(0, e, 0xB1, 0xf, 0xf, true);
;     int f = o2 ? c : a, g = o2 ? a : c;
;     f += __builtin_amdgcn_update_dpp(0, g, 0x4E, 0xf, 0xf, true);
;     f += __builtin_amdgcn_update_dpp(0, f, 0x124, 0xf, 0xf, true);
;     f += __builtin_amdgcn_update_dpp(0, f, 0x128, 0xf, 0xf, true);
; __device__ __forceinline__ void peer3_dots(const u4 (&R)[PG][2], const u4 (&xq)[2], int sx15, LAS int* redrow, int g) {
;     ...
;     for (int k = 0; k < 4; ++k) { int a = 0, ah = 0;
; #pragma unroll
;         for (int q = 0; q < 4; ++q) { const unsigned w = R[k][0][q];
;             a = __builtin_amdgcn_sdot4((int)(w & 0x0f0f0f0fu), (int)xq[0][q], a, false); ah = __builtin_amdgcn_sdot4((int)(w & 0xf0f0f0f0u), (int)xq[1][q], ah, false); }
;         d[k] = 32 * a + 2 * ah - sx15; }
;     u4 w; w.x = (unsigned)d[0]; w.y = (unsigned)d[1]; w.z = (unsigned)d[2]; w.w = (unsigned)d[3];
;     *(LAS u4*)(redrow + 4 * g) = w;
.Lq_swret2:
	s_waitcnt vmcnt(8)
	s_bitcmp1_b32 s62, 3
	s_cbranch_scc1 .Lq_fin2
.Lq_finret2:
	v_and_b32_e32 v95, 0xf0f0f0f, v32
	v_and_b32_e32 v99, 0xf0f0f0f0, v32
	v_and_b32_e32 v96, 0xf0f0f0f, v33
	v_and_b32_e32 v100, 0xf0f0f0f0, v33
	v_dot4_i32_i8 v103, v95, v64, 0
	v_dot4_i32_i8 v104, v99, v68, 0
	v_and_b32_e32 v97, 0xf0f0f0f, v34
	v_and_b32_e32 v101, 0xf0f0f0f0, v34
	v_dot4_i32_i8 v103, v96, v65, v103
	v_dot4_i32_i8 v104, v100, v69, v104
	v_and_b32_e32 v98, 0xf0f0f0f, v35
	v_and_b32_e32 v102, 0xf0f0f0f0, v35
	v_dot4_i32_i8 v103, v97, v66, v103
	v_dot4_i32_i8 v104, v101, v70, v104
	v_dot4_i32_i8 v103, v98, v67, v103
	v_dot4_i32_i8 v104, v102, v71, v104
	v_and_b32_e32 v95, 0xf0f0f0f, v36
	v_and_b32_e32 v99, 0xf0f0f0f0, v36
	v_and_b32_e32 v96, 0xf0f0f0f, v37
	v_and_b32_e32 v100, 0xf0f0f0f0, v37
	v_lshl_add_u32 v105, v103, 4, v104
	v_lshl_add_u32 v91, v105, 1, v72
	v_dot4_i32_i8 v126, v95, v64, 0
	v_dot4_i32_i8 v127, v99, v68, 0
	v_and_b32_e32 v97, 0xf0f0f0f, v38
	v_and_b32_e32 v101, 0xf0f0f0f0, v38
	v_dot4_i32_i8 v126, v96, v65, v126
	v_dot4_i32_i8 v127, v100, v69, v127
	v_and_b32_e32 v98, 0xf0f0f0f, v39
	v_and_b32_e32 v102, 0xf0f0f0f0, v39
	v_dot4_i32_i8 v126, v97, v66, v126
	v_dot4_i32_i8 v127, v101, v70, v127
	v_dot4_i32_i8 v126, v98, v67, v126
	v_dot4_i32_i8 v127, v102, v71, v127
	v_and_b32_e32 v95, 0xf0f0f0f, v40
	v_and_b32_e32 v99, 0xf0f0f0f0, v40
	v_and_b32_e32 v96, 0xf0f0f0f, v41
	v_and_b32_e32 v100, 0xf0f0f0f0, v41
	v_lshl_add_u32 v105, v126, 4, v127
	v_lshl_add_u32 v92, v105, 1, v72
	v_dot4_i32_i8 v103, v95, v64, 0
	v_dot4_i32_i8 v104, v99, v68, 0
	v_and_b32_e32 v97, 0xf0f0f0f, v42
	v_and_b32_e32 v101, 0xf0f0f0f0, v42
	v_dot4_i32_i8 v103, v96, v65, v103
	v_dot4_i32_i8 v104, v100, v69, v104
	v_and_b32_e32 v98, 0xf0f0f0f, v43
	v_and_b32_e32 v102, 0xf0f0f0f0, v43
	v_dot4_i32_i8 v103, v97, v66, v103
	v_dot4_i32_i8 v104, v101, v70, v104
	v_dot4_i32_i8 v103, v98, v67, v103
	v_dot4_i32_i8 v104, v102, v71, v104
	v_and_b32_e32 v95, 0xf0f0f0f, v44
	v_and_b32_e32 v99, 0xf0f0f0f0, v44
	v_and_b32_e32 v96, 0xf0f0f0f, v45
	v_and_b32_e32 v100, 0xf0f0f0f0, v45
	v_lshl_add_u32 v105, v103, 4, v104
	v_lshl_add_u32 v93, v105, 1, v72
	v_dot4_i32_i8 v126, v95, v64, 0
	v_dot4_i32_i8 v127, v99, v68, 0
	v_and_b32_e32 v97, 0xf0f0f0f, v46
	v_and_b32_e32 v101, 0xf0f0f0f0, v46
	v_dot4_i32_i8 v126, v96, v65, v126
	v_dot4_i32_i8 v127, v100, v69, v127
	v_and_b32_e32 v98, 0xf0f0f0f, v47
	v_and_b32_e32 v102, 0xf0f0f0f0, v47
	v_dot4_i32_i8 v126, v97, v66, v126
	v_dot4_i32_i8 v127, v101, v70, v127
	v_dot4_i32_i8 v126, v98, v67, v126
	v_dot4_i32_i8 v127, v102, v71, v127
	v_readlane_b32 s36, v75, 20
	v_readlane_b32 s5, v75, 21
	v_readlane_b32 s6, v75, 22
	v_lshl_add_u32 v105, v126, 4, v127
	v_lshl_add_u32 v94, v105, 1, v72
	v_cndmask_b32_e64 v107, v92, v91, s[38:39]
	v_cndmask_b32_e64 v109, v94, v93, s[38:39]
	v_cndmask_b32_e64 v106, v91, v92, s[38:39]
	v_cndmask_b32_e64 v108, v93, v94, s[38:39]
	v_add_u32_dpp v106, v107, v106 quad_perm:[1,0,3,2] row_mask:0xf bank_mask:0xf
	v_add_u32_dpp v108, v109, v108 quad_perm:[1,0,3,2] row_mask:0xf bank_mask:0xf
	v_readlane_b32 s7, v75, 23
	v_cndmask_b32_e64 v111, v108, v106, s[42:43]
	v_cndmask_b32_e64 v110, v106, v108, s[42:43]
	v_add_u32_e32 v113, s36, v206
	v_add_u32_e32 v114, s5, v206
	v_add_u32_dpp v110, v111, v110 quad_perm:[2,3,0,1] row_mask:0xf bank_mask:0xf
	v_add_u32_e32 v115, s6, v206
	v_add_u32_e32 v116, s7, v206
	v_add_u32_dpp v110, v110, v110 row_ror:4 row_mask:0xf bank_mask:0xf
	global_load_dwordx4 v[16:19], v113, s[52:53]
	global_load_dwordx4 v[20:23], v114, s[52:53]
	v_add_u32_dpp v110, v110, v110 row_ror:8 row_mask:0xf bank_mask:0xf
	global_load_dwordx4 v[24:27], v115, s[52:53]
	global_load_dwordx4 v[28:31], v116, s[52:53]
	s_lshl_b64 exec, s[22:23], 8
	v_mov_b32_e32 v83, v110
	v_mov_b32_e32 v87, s10
	s_mov_b64 exec, -1
.Lq_g3:
	s_add_u32 s11, s34, 12
	s_cmp_ge_u32 s11, s28
	s_cbranch_scc1 .Lq_end
	s_cmp_gt_u32 s50, 31
	s_cbranch_scc1 .Lq_stdg3
	s_add_u32 s36, s11, 20
	v_readlane_b32 s4, v81, s50
	s_cmp_lt_u32 s4, s36
	s_cbranch_scc1 .Lq_stxg3

; #define LAS __attribute__((address_space(3)))
; __device__ __forceinline__ int wave_isum4_t(const int (&d)[4], int lane) {
;     const bool o1 = lane & 1, o2 = lane & 2;
;     int a = o1 ? d[1] : d[0], b = o1 ? d[0] : d[1], c = o1 ? d[3] : d[2], e = o1 ? d[2] : d[3];
;     a += __builtin_amdgcn_update_dpp(0, b, 0xB1, 0xf, 0xf, true);
;     c += __builtin_amdgcn_update_dpp(0, e, 0xB1, 0xf, 0xf, true);
;     int f = o2 ? c : a, g = o2 ? a : c;
;     f += __builtin_amdgcn_update_dpp(0, g, 0x4E, 0xf, 0xf, true);
;     f += __builtin_amdgcn_update_dpp(0, f, 0x124, 0xf, 0xf, true);
;     f += __builtin_amdgcn_update_dpp(0, f, 0x128, 0xf, 0xf, true);
; __device__ __forceinline__ void peer3_dots(const u4 (&R)[PG][2], const u4 (&xq)[2], int sx15, LAS int* redrow, int g) {
;     ...
;     for (int k = 0; k < 4; ++k) { int a = 0, ah = 0;
; #pragma unroll
;         for (int q = 0; q < 4; ++q) { const unsigned w = R[k][0][q];
;             a = __builtin_amdgcn_sdot4((int)(w & 0x0f0f0f0fu), (int)xq[0][q], a, false); ah = __builtin_amdgcn_sdot4((int)(w & 0xf0f0f0f0u), (int)xq[1][q], ah, false); }
;         d[k] = 32 * a + 2 * ah - sx15; }
;     u4 w; w.x = (unsigned)d[0]; w.y = (unsigned)d[1]; w.z = (unsigned)d[2]; w.w = (unsigned)d[3];
;     *(LAS u4*)(redrow + 4 * g) = w;
.Lq_swret3:
	s_waitcnt vmcnt(8)
	s_bitcmp1_b32 s62, 0
	s_cbranch_scc1 .Lq_fin3
.Lq_finret3:
	v_and_b32_e32 v95, 0xf0f0f0f, v48
	v_and_b32_e32 v99, 0xf0f0f0f0, v48
	v_and_b32_e32 v96, 0xf0f0f0f, v49
	v_and_b32_e32 v100, 0xf0f0f0f0, v49
	v_dot4_i32_i8 v103, v95, v64, 0
	v_dot4_i32_i8 v104, v99, v68, 0
	v_and_b32_e32 v97, 0xf0f0f0f, v50
	v_and_b32_e32 v101, 0xf0f0f0f0, v50
	v_dot4_i32_i8 v103, v96, v65, v103
	v_dot4_i32_i8 v104, v100, v69, v104
	v_and_b32_e32 v98, 0xf0f0f0f, v51
	v_and_b32_e32 v102, 0xf0f0f0f0, v51
	v_dot4_i32_i8 v103, v97, v66, v103
	v_dot4_i32_i8 v104, v101, v70, v104
	v_dot4_i32_i8 v103, v98, v67, v103
	v_dot4_i32_i8 v104, v102, v71, v104
	v_and_b32_e32 v95, 0xf0f0f0f, v52
	v_and_b32_e32 v99, 0xf0f0f0f0, v52
	v_and_b32_e32 v96, 0xf0f0f0f, v53
	v_and_b32_e32 v100, 0xf0f0f0f0, v53
	v_lshl_add_u32 v105, v103, 4, v104
	v_lshl_add_u32 v91, v105, 1, v72
	v_dot4_i32_i8 v126, v95, v64, 0
	v_dot4_i32_i8 v127, v99, v68, 0
	v_and_b32_e32 v97, 0xf0f0f0f, v54
	v_and_b32_e32 v101, 0xf0f0f0f0, v54
	v_dot4_i32_i8 v126, v96, v65, v126
	v_dot4_i32_i8 v127, v100, v69, v127
	v_and_b32_e32 v98, 0xf0f0f0f, v55
	v_and_b32_e32 v102, 0xf0f0f0f0, v55
	v_dot4_i32_i8 v126, v97, v66, v126
	v_dot4_i32_i8 v127, v101, v70, v127
	v_dot4_i32_i8 v126, v98, v67, v126
	v_dot4_i32_i8 v127, v102, v71, v127
	v_and_b32_e32 v95, 0xf0f0f0f, v56
	v_and_b32_e32 v99, 0xf0f0f0f0, v56
	v_and_b32_e32 v96, 0xf0f0f0f, v57
	v_and_b32_e32 v100, 0xf0f0f0f0, v57
	v_lshl_add_u32 v105, v126, 4, v127
	v_lshl_add_u32 v92, v105, 1, v72
	v_dot4_i32_i8 v103, v95, v64, 0
	v_dot4_i32_i8 v104, v99, v68, 0
	v_and_b32_e32 v97, 0xf0f0f0f, v58
	v_and_b32_e32 v101, 0xf0f0f0f0, v58
	v_dot4_i32_i8 v103, v96, v65, v103
	v_dot4_i32_i8 v104, v100, v69, v104
	v_and_b32_e32 v98, 0xf0f0f0f, v59
	v_and_b32_e32 v102, 0xf0f0f0f0, v59
	v_dot4_i32_i8 v103, v97, v66, v103
	v_dot4_i32_i8 v104, v101, v70, v104
	v_dot4_i32_i8 v103, v98, v67, v103
	v_dot4_i32_i8 v104, v102, v71, v104
	v_and_b32_e32 v95, 0xf0f0f0f, v60
	v_and_b32_e32 v99, 0xf0f0f0f0, v60
	v_and_b32_e32 v96, 0xf0f0f0f, v61
	v_and_b32_e32 v100, 0xf0f0f0f0, v61
	v_lshl_add_u32 v105, v103, 4, v104
	v_lshl_add_u32 v93, v105, 1, v72
	v_dot4_i32_i8 v126, v95, v64, 0
	v_dot4_i32_i8 v127, v99, v68, 0
	v_and_b32_e32 v97, 0xf0f0f0f, v62
	v_and_b32_e32 v101, 0xf0f0f0f0, v62
	v_dot4_i32_i8 v126, v96, v65, v126
	v_dot4_i32_i8 v127, v100, v69, v127
	v_and_b32_e32 v98, 0xf0f0f0f, v63
	v_and_b32_e32 v102, 0xf0f0f0f0, v63
	v_dot4_i32_i8 v126, v97, v66, v126
	v_dot4_i32_i8 v127, v101, v70, v127
	v_dot4_i32_i8 v126, v98, v67, v126
	v_dot4_i32_i8 v127, v102, v71, v127
	v_readlane_b32 s36, v75, 24
	v_readlane_b32 s5, v75, 25
	v_readlane_b32 s6, v75, 26
	v_lshl_add_u32 v105, v126, 4, v127
	v_lshl_add_u32 v94, v105, 1, v72
	v_cndmask_b32_e64 v107, v92, v91, s[38:39]
	v_cndmask_b32_e64 v109, v94, v93, s[38:39]
	v_cndmask_b32_e64 v106, v91, v92, s[38:39]
	v_cndmask_b32_e64 v108, v93, v94, s[38:39]
	v_add_u32_dpp v106, v107, v106 quad_perm:[1,0,3,2] row_mask:0xf bank_mask:0xf
	v_add_u32_dpp v108, v109, v108 quad_perm:[1,0,3,2] row_mask:0xf bank_mask:0xf
	v_readlane_b32 s7, v75, 27
	v_cndmask_b32_e64 v111, v108, v106, s[42:43]
	v_cndmask_b32_e64 v110, v106, v108, s[42:43]
	v_add_u32_e32 v113, s36, v206
	v_add_u32_e32 v114, s5, v206
	v_add_u32_dpp v110, v111, v110 quad_perm:[2,3,0,1] row_mask:0xf bank_mask:0xf
	v_add_u32_e32 v115, s6, v206
	v_add_u32_e32 v116, s7, v206
	v_add_u32_dpp v110, v110, v110 row_ror:4 row_mask:0xf bank_mask:0xf
	global_load_dwordx4 v[32:35], v113, s[52:53]
	global_load_dwordx4 v[36:39], v114, s[52:53]
	v_add_u32_dpp v110, v110, v110 row_ror:8 row_mask:0xf bank_mask:0xf
	global_load_dwordx4 v[40:43], v115, s[52:53]
	global_load_dwordx4 v[44:47], v116, s[52:53]
	s_lshl_b64 exec, s[22:23], 12
	v_mov_b32_e32 v83, v110
	v_mov_b32_e32 v87, s10
	s_mov_b64 exec, -1
.Lq_g4:
	s_add_u32 s11, s34, 16
	s_cmp_ge_u32 s11, s28
	s_cbranch_scc1 .Lq_end
	s_cmp_gt_u32 s50, 31
	s_cbranch_scc1 .Lq_stdg4
	s_add_u32 s36, s11, 20
	v_readlane_b32 s4, v81, s50
	s_cmp_lt_u32 s4, s36
	s_cbranch_scc1 .Lq_stxg4

; #define LAS __attribute__((address_space(3)))
; __device__ __forceinline__ int wave_isum4_t(const int (&d)[4], int lane) {
;     const bool o1 = lane & 1, o2 = lane & 2;
;     int a = o1 ? d[1] : d[0], b = o1 ? d[0] : d[1], c = o1 ? d[3] : d[2], e = o1 ? d[2] : d[3];
;     a += __builtin_amdgcn_update_dpp(0, b, 0xB1, 0xf, 0xf, true);
;     c += __builtin_amdgcn_update_dpp(0, e, 0xB1, 0xf, 0xf, true);
;     int f = o2 ? c : a, g = o2 ? a : c;
;     f += __builtin_amdgcn_update_dpp(0, g, 0x4E, 0xf, 0xf, true);
;     f += __builtin_amdgcn_update_dpp(0, f, 0x124, 0xf, 0xf, true);
;     f += __builtin_amdgcn_update_dpp(0, f, 0x128, 0xf, 0xf, true);
; __device__ __forceinline__ void peer3_dots(const u4 (&R)[PG][2], const u4 (&xq)[2], int sx15, LAS int* redrow, int g) {
;     ...
;     for (int k = 0; k < 4; ++k) { int a = 0, ah = 0;
; #pragma unroll
;         for (int q = 0; q < 4; ++q) { const unsigned w = R[k][0][q];
;             a = __builtin_amdgcn_sdot4((int)(w & 0x0f0f0f0fu), (int)xq[0][q], a, false); ah = __builtin_amdgcn_sdot4((int)(w & 0xf0f0f0f0u), (int)xq[1][q], ah, false); }
;         d[k] = 32 * a + 2 * ah - sx15; }
;     u4 w; w.x = (unsigned)d[0]; w.y = (unsigned)d[1]; w.z = (unsigned)d[2]; w.w = (unsigned)d[3];
;     *(LAS u4*)(redrow + 4 * g) = w;
.Lq_finret4:
	v_and_b32_e32 v95, 0xf0f0f0f, v0
	v_and_b32_e32 v99, 0xf0f0f0f0, v0
	v_and_b32_e32 v96, 0xf0f0f0f, v1
	v_and_b32_e32 v100, 0xf0f0f0f0, v1
	v_dot4_i32_i8 v103, v95, v64, 0
	v_dot4_i32_i8 v104, v99, v68, 0
	v_and_b32_e32 v97, 0xf0f0f0f, v2
	v_and_b32_e32 v101, 0xf0f0f0f0, v2
	v_dot4_i32_i8 v103, v96, v65, v103
	v_dot4_i32_i8 v104, v100, v69, v104
	v_and_b32_e32 v98, 0xf0f0f0f, v3
	v_and_b32_e32 v102, 0xf0f0f0f0, v3
	v_dot4_i32_i8 v103, v97, v66, v103
	v_dot4_i32_i8 v104, v101, v70, v104
	v_dot4_i32_i8 v103, v98, v67, v103
	v_dot4_i32_i8 v104, v102, v71, v104
	v_and_b32_e32 v95, 0xf0f0f0f, v4
	v_and_b32_e32 v99, 0xf0f0f0f0, v4
	v_and_b32_e32 v96, 0xf0f0f0f, v5
	v_and_b32_e32 v100, 0xf0f0f0f0, v5
	v_lshl_add_u32 v105, v103, 4, v104
	v_lshl_add_u32 v91, v105, 1, v72
	v_dot4_i32_i8 v126, v95, v64, 0
	v_dot4_i32_i8 v127, v99, v68, 0
	v_and_b32_e32 v97, 0xf0f0f0f, v6
	v_and_b32_e32 v101, 0xf0f0f0f0, v6
	v_dot4_i32_i8 v126, v96, v65, v126
	v_dot4_i32_i8 v127, v100, v69, v127
	v_and_b32_e32 v98, 0xf0f0f0f, v7
	v_and_b32_e32 v102, 0xf0f0f0f0, v7
	v_dot4_i32_i8 v126, v97, v66, v126
	v_dot4_i32_i8 v127, v101, v70, v127
	v_dot4_i32_i8 v126, v98, v67, v126
	v_dot4_i32_i8 v127, v102, v71, v127
	v_and_b32_e32 v95, 0xf0f0f0f, v8
	v_and_b32_e32 v99, 0xf0f0f0f0, v8
	v_and_b32_e32 v96, 0xf0f0f0f, v9
	v_and_b32_e32 v100, 0xf0f0f0f0, v9
	v_lshl_add_u32 v105, v126, 4, v127
	v_lshl_add_u32 v92, v105, 1, v72
	v_dot4_i32_i8 v103, v95, v64, 0
	v_dot4_i32_i8 v104, v99, v68, 0
	v_and_b32_e32 v97, 0xf0f0f0f, v10
	v_and_b32_e32 v101, 0xf0f0f0f0, v10
	v_dot4_i32_i8 v103, v96, v65, v103
	v_dot4_i32_i8 v104, v100, v69, v104
	v_and_b32_e32 v98, 0xf0f0f0f, v11
	v_and_b32_e32 v102, 0xf0f0f0f0, v11
	v_dot4_i32_i8 v103, v97, v66, v103
	v_dot4_i32_i8 v104, v101, v70, v104
	v_dot4_i32_i8 v103, v98, v67, v103
	v_dot4_i32_i8 v104, v102, v71, v104
	v_and_b32_e32 v95, 0xf0f0f0f, v12
	v_and_b32_e32 v99, 0xf0f0f0f0, v12
	v_and_b32_e32 v96, 0xf0f0f0f, v13
	v_and_b32_e32 v100, 0xf0f0f0f0, v13
	v_lshl_add_u32 v105, v103, 4, v104
	v_lshl_add_u32 v93, v105, 1, v72
	v_dot4_i32_i8 v126, v95, v64, 0
	v_dot4_i32_i8 v127, v99, v68, 0
	v_and_b32_e32 v97, 0xf0f0f0f, v14
	v_and_b32_e32 v101, 0xf0f0f0f0, v14
	v_dot4_i32_i8 v126, v96, v65, v126
	v_dot4_i32_i8 v127, v100, v69, v127
	v_and_b32_e32 v98, 0xf0f0f0f, v15
	v_and_b32_e32 v102, 0xf0f0f0f0, v15
	v_dot4_i32_i8 v126, v97, v66, v126
	v_dot4_i32_i8 v127, v101, v70, v127
	v_dot4_i32_i8 v126, v98, v67, v126
	v_dot4_i32_i8 v127, v102, v71, v127
	v_readlane_b32 s36, v75, 28
	v_readlane_b32 s5, v75, 29
	v_readlane_b32 s6, v75, 30
	v_lshl_add_u32 v105, v126, 4, v127
	v_lshl_add_u32 v94, v105, 1, v72
	v_cndmask_b32_e64 v107, v92, v91, s[38:39]
	v_cndmask_b32_e64 v109, v94, v93, s[38:39]
	v_cndmask_b32_e64 v106, v91, v92, s[38:39]
	v_cndmask_b32_e64 v108, v93, v94, s[38:39]
	v_add_u32_dpp v106, v107, v106 quad_perm:[1,0,3,2] row_mask:0xf bank_mask:0xf
	v_add_u32_dpp v108, v109, v108 quad_perm:[1,0,3,2] row_mask:0xf bank_mask:0xf
	v_readlane_b32 s7, v75, 31
	v_cndmask_b32_e64 v111, v108, v106, s[42:43]
	v_cndmask_b32_e64 v110, v106, v108, s[42:43]
	v_add_u32_e32 v113, s36, v206
	v_add_u32_e32 v114, s5, v206
	v_add_u32_dpp v110, v111, v110 quad_perm:[2,3,0,1] row_mask:0xf bank_mask:0xf
	v_add_u32_e32 v115, s6, v206
	v_add_u32_e32 v116, s7, v206
	v_add_u32_dpp v110, v110, v110 row_ror:4 row_mask:0xf bank_mask:0xf
	global_load_dwordx4 v[48:51], v113, s[52:53]
	global_load_dwordx4 v[52:55], v114, s[52:53]
	v_add_u32_dpp v110, v110, v110 row_ror:8 row_mask:0xf bank_mask:0xf
	global_load_dwordx4 v[56:59], v115, s[52:53]
	global_load_dwordx4 v[60:63], v116, s[52:53]
	s_mov_b64 exec, s[22:23]
	v_mov_b32_e32 v84, v110
	v_mov_b32_e32 v88, s10
	s_mov_b64 exec, -1
.Lq_g5:
	s_add_u32 s11, s34, 20
	s_cmp_ge_u32 s11, s28
	s_cbranch_scc1 .Lq_end
	s_cmp_gt_u32 s50, 31
	s_cbranch_scc1 .Lq_stdg5
	s_add_u32 s36, s11, 20
	v_readlane_b32 s4, v81, s50
	s_cmp_lt_u32 s4, s36
	s_cbranch_scc1 .Lq_stxg5

; #define LAS __attribute__((address_space(3)))
; __device__ __forceinline__ int wave_isum4_t(const int (&d)[4], int lane) {
;     const bool o1 = lane & 1, o2 = lane & 2;
;     int a = o1 ? d[1] : d[0], b = o1 ? d[0] : d[1], c = o1 ? d[3] : d[2], e = o1 ? d[2] : d[3];
;     a += __builtin_amdgcn_update_dpp(0, b, 0xB1, 0xf, 0xf, true);
;     c += __builtin_amdgcn_update_dpp(0, e, 0xB1, 0xf, 0xf, true);
;     int f = o2 ? c : a, g = o2 ? a : c;
;     f += __builtin_amdgcn_update_dpp(0, g, 0x4E, 0xf, 0xf, true);
;     f += __builtin_amdgcn_update_dpp(0, f, 0x124, 0xf, 0xf, true);
;     f += __builtin_amdgcn_update_dpp(0, f, 0x128, 0xf, 0xf, true);
; __device__ __forceinline__ void peer3_dots(const u4 (&R)[PG][2], const u4 (&xq)[2], int sx15, LAS int* redrow, int g) {
;     ...
;     for (int k = 0; k < 4; ++k) { int a = 0, ah = 0;
; #pragma unroll
;         for (int q = 0; q < 4; ++q) { const unsigned w = R[k][0][q];
;             a = __builtin_amdgcn_sdot4((int)(w & 0x0f0f0f0fu), (int)xq[0][q], a, false); ah = __builtin_amdgcn_sdot4((int)(w & 0xf0f0f0f0u), (int)xq[1][q], ah, false); }
;         d[k] = 32 * a + 2 * ah - sx15; }
;     u4 w; w.x = (unsigned)d[0]; w.y = (unsigned)d[1]; w.z = (unsigned)d[2]; w.w = (unsigned)d[3];
;     *(LAS u4*)(redrow + 4 * g) = w;
.Lq_finret5:
	v_and_b32_e32 v95, 0xf0f0f0f, v16
	v_and_b32_e32 v99, 0xf0f0f0f0, v16
	v_and_b32_e32 v96, 0xf0f0f0f, v17
	v_and_b32_e32 v100, 0xf0f0f0f0, v17
	v_dot4_i32_i8 v103, v95, v64, 0
	v_dot4_i32_i8 v104, v99, v68, 0
	v_and_b32_e32 v97, 0xf0f0f0f, v18
	v_and_b32_e32 v101, 0xf0f0f0f0, v18
	v_dot4_i32_i8 v103, v96, v65, v103
	v_dot4_i32_i8 v104, v100, v69, v104
	v_and_b32_e32 v98, 0xf0f0f0f, v19
	v_and_b32_e32 v102, 0xf0f0f0f0, v19
	v_dot4_i32_i8 v103, v97, v66, v103
	v_dot4_i32_i8 v104, v101, v70, v104
	v_dot4_i32_i8 v103, v98, v67, v103
	v_dot4_i32_i8 v104, v102, v71, v104
	v_and_b32_e32 v95, 0xf0f0f0f, v20
	v_and_b32_e32 v99, 0xf0f0f0f0, v20
	v_and_b32_e32 v96, 0xf0f0f0f, v21
	v_and_b32_e32 v100, 0xf0f0f0f0, v21
	v_lshl_add_u32 v105, v103, 4, v104
	v_lshl_add_u32 v91, v105, 1, v72
	v_dot4_i32_i8 v126, v95, v64, 0
	v_dot4_i32_i8 v127, v99, v68, 0
	v_and_b32_e32 v97, 0xf0f0f0f, v22
	v_and_b32_e32 v101, 0xf0f0f0f0, v22
	v_dot4_i32_i8 v126, v96, v65, v126
	v_dot4_i32_i8 v127, v100, v69, v127
	v_and_b32_e32 v98, 0xf0f0f0f, v23
	v_and_b32_e32 v102, 0xf0f0f0f0, v23
	v_dot4_i32_i8 v126, v97, v66, v126
	v_dot4_i32_i8 v127, v101, v70, v127
	v_dot4_i32_i8 v126, v98, v67, v126
	v_dot4_i32_i8 v127, v102, v71, v127
	v_and_b32_e32 v95, 0xf0f0f0f, v24
	v_and_b32_e32 v99, 0xf0f0f0f0, v24
	v_and_b32_e32 v96, 0xf0f0f0f, v25
	v_and_b32_e32 v100, 0xf0f0f0f0, v25
	v_lshl_add_u32 v105, v126, 4, v127
	v_lshl_add_u32 v92, v105, 1, v72
	v_dot4_i32_i8 v103, v95, v64, 0
	v_dot4_i32_i8 v104, v99, v68, 0
	v_and_b32_e32 v97, 0xf0f0f0f, v26
	v_and_b32_e32 v101, 0xf0f0f0f0, v26
	v_dot4_i32_i8 v103, v96, v65, v103
	v_dot4_i32_i8 v104, v100, v69, v104
	v_and_b32_e32 v98, 0xf0f0f0f, v27
	v_and_b32_e32 v102, 0xf0f0f0f0, v27
	v_dot4_i32_i8 v103, v97, v66, v103
	v_dot4_i32_i8 v104, v101, v70, v104
	v_dot4_i32_i8 v103, v98, v67, v103
	v_dot4_i32_i8 v104, v102, v71, v104
	v_and_b32_e32 v95, 0xf0f0f0f, v28
	v_and_b32_e32 v99, 0xf0f0f0f0, v28
	v_and_b32_e32 v96, 0xf0f0f0f, v29
	v_and_b32_e32 v100, 0xf0f0f0f0, v29
	v_lshl_add_u32 v105, v103, 4, v104
	v_lshl_add_u32 v93, v105, 1, v72
	v_dot4_i32_i8 v126, v95, v64, 0
	v_dot4_i32_i8 v127, v99, v68, 0
	v_and_b32_e32 v97, 0xf0f0f0f, v30
	v_and_b32_e32 v101, 0xf0f0f0f0, v30
	v_dot4_i32_i8 v126, v96, v65, v126
	v_dot4_i32_i8 v127, v100, v69, v127
	v_and_b32_e32 v98, 0xf0f0f0f, v31
	v_and_b32_e32 v102, 0xf0f0f0f0, v31
	v_dot4_i32_i8 v126, v97, v66, v126
	v_dot4_i32_i8 v127, v101, v70, v127
	v_dot4_i32_i8 v126, v98, v67, v126
	v_dot4_i32_i8 v127, v102, v71, v127
	v_readlane_b32 s36, v75, 32
	v_readlane_b32 s5, v75, 33
	v_readlane_b32 s6, v75, 34
	v_lshl_add_u32 v105, v126, 4, v127
	v_lshl_add_u32 v94, v105, 1, v72
	v_cndmask_b32_e64 v107, v92, v91, s[38:39]
	v_cndmask_b32_e64 v109, v94, v93, s[38:39]
	v_cndmask_b32_e64 v106, v91, v92, s[38:39]
	v_cndmask_b32_e64 v108, v93, v94, s[38:39]
	v_add_u32_dpp v106, v107, v106 quad_perm:[1,0,3,2] row_mask:0xf bank_mask:0xf
	v_add_u32_dpp v108, v109, v108 quad_perm:[1,0,3,2] row_mask:0xf bank_mask:0xf
	v_readlane_b32 s7, v75, 35
	v_cndmask_b32_e64 v111, v108, v106, s[42:43]
	v_cndmask_b32_e64 v110, v106, v108, s[42:43]
	v_add_u32_e32 v113, s36, v206
	v_add_u32_e32 v114, s5, v206
	v_add_u32_dpp v110, v111, v110 quad_perm:[2,3,0,1] row_mask:0xf bank_mask:0xf
	v_add_u32_e32 v115, s6, v206
	v_add_u32_e32 v116, s7, v206
	v_add_u32_dpp v110, v110, v110 row_ror:4 row_mask:0xf bank_mask:0xf
	global_load_dwordx4 v[0:3], v113, s[52:53]
	global_load_dwordx4 v[4:7], v114, s[52:53]
	v_add_u32_dpp v110, v110, v110 row_ror:8 row_mask:0xf bank_mask:0xf
	global_load_dwordx4 v[8:11], v115, s[52:53]
	global_load_dwordx4 v[12:15], v116, s[52:53]
	s_lshl_b64 exec, s[22:23], 4
	v_mov_b32_e32 v84, v110
	v_mov_b32_e32 v88, s10
	s_mov_b64 exec, -1
.Lq_g6:
	s_add_u32 s11, s34, 24
	s_cmp_ge_u32 s11, s28
	s_cbranch_scc1 .Lq_end
	s_cmp_gt_u32 s50, 31
	s_cbranch_scc1 .Lq_stdg6
	s_add_u32 s36, s11, 20
	v_readlane_b32 s4, v81, s50
	s_cmp_lt_u32 s4, s36
	s_cbranch_scc1 .Lq_stxg6

; #define LAS __attribute__((address_space(3)))
; __device__ __forceinline__ int wave_isum4_t(const int (&d)[4], int lane) {
;     const bool o1 = lane & 1, o2 = lane & 2;
;     int a = o1 ? d[1] : d[0], b = o1 ? d[0] : d[1], c = o1 ? d[3] : d[2], e = o1 ? d[2] : d[3];
;     a += __builtin_amdgcn_update_dpp(0, b, 0xB1, 0xf, 0xf, true);
;     c += __builtin_amdgcn_update_dpp(0, e, 0xB1, 0xf, 0xf, true);
;     int f = o2 ? c : a, g = o2 ? a : c;
;     f += __builtin_amdgcn_update_dpp(0, g, 0x4E, 0xf, 0xf, true);
;     f += __builtin_amdgcn_update_dpp(0, f, 0x124, 0xf, 0xf, true);
;     f += __builtin_amdgcn_update_dpp(0, f, 0x128, 0xf, 0xf, true);
; __device__ __forceinline__ void peer3_dots(const u4 (&R)[PG][2], const u4 (&xq)[2], int sx15, LAS int* redrow, int g) {
;     ...
;     for (int k = 0; k < 4; ++k) { int a = 0, ah = 0;
; #pragma unroll
;         for (int q = 0; q < 4; ++q) { const unsigned w = R[k][0][q];
;             a = __builtin_amdgcn_sdot4((int)(w & 0x0f0f0f0fu), (int)xq[0][q], a, false); ah = __builtin_amdgcn_sdot4((int)(w & 0xf0f0f0f0u), (int)xq[1][q], ah, false); }
;         d[k] = 32 * a + 2 * ah - sx15; }
;     u4 w; w.x = (unsigned)d[0]; w.y = (unsigned)d[1]; w.z = (unsigned)d[2]; w.w = (unsigned)d[3];
;     *(LAS u4*)(redrow + 4 * g) = w;
.Lq_finret6:
	v_and_b32_e32 v95, 0xf0f0f0f, v32
	v_and_b32_e32 v99, 0xf0f0f0f0, v32
	v_and_b32_e32 v96, 0xf0f0f0f, v33
	v_and_b32_e32 v100, 0xf0f0f0f0, v33
	v_dot4_i32_i8 v103, v95, v64, 0
	v_dot4_i32_i8 v104, v99, v68, 0
	v_and_b32_e32 v97, 0xf0f0f0f, v34
	v_and_b32_e32 v101, 0xf0f0f0f0, v34
	v_dot4_i32_i8 v103, v96, v65, v103
	v_dot4_i32_i8 v104, v100, v69, v104
	v_and_b32_e32 v98, 0xf0f0f0f, v35
	v_and_b32_e32 v102, 0xf0f0f0f0, v35
	v_dot4_i32_i8 v103, v97, v66, v103
	v_dot4_i32_i8 v104, v101, v70, v104
	v_dot4_i32_i8 v103, v98, v67, v103
	v_dot4_i32_i8 v104, v102, v71, v104
	v_and_b32_e32 v95, 0xf0f0f0f, v36
	v_and_b32_e32 v99, 0xf0f0f0f0, v36
	v_and_b32_e32 v96, 0xf0f0f0f, v37
	v_and_b32_e32 v100, 0xf0f0f0f0, v37
	v_lshl_add_u32 v105, v103, 4, v104
	v_lshl_add_u32 v91, v105, 1, v72
	v_dot4_i32_i8 v126, v95, v64, 0
	v_dot4_i32_i8 v127, v99, v68, 0
	v_and_b32_e32 v97, 0xf0f0f0f, v38
	v_and_b32_e32 v101, 0xf0f0f0f0, v38
	v_dot4_i32_i8 v126, v96, v65, v126
	v_dot4_i32_i8 v127, v100, v69, v127
	v_and_b32_e32 v98, 0xf0f0f0f, v39
	v_and_b32_e32 v102, 0xf0f0f0f0, v39
	v_dot4_i32_i8 v126, v97, v66, v126
	v_dot4_i32_i8 v127, v101, v70, v127
	v_dot4_i32_i8 v126, v98, v67, v126
	v_dot4_i32_i8 v127, v102, v71, v127
	v_and_b32_e32 v95, 0xf0f0f0f, v40
	v_and_b32_e32 v99, 0xf0f0f0f0, v40
	v_and_b32_e32 v96, 0xf0f0f0f, v41
	v_and_b32_e32 v100, 0xf0f0f0f0, v41
	v_lshl_add_u32 v105, v126, 4, v127
	v_lshl_add_u32 v92, v105, 1, v72
	v_dot4_i32_i8 v103, v95, v64, 0
	v_dot4_i32_i8 v104, v99, v68, 0
	v_and_b32_e32 v97, 0xf0f0f0f, v42
	v_and_b32_e32 v101, 0xf0f0f0f0, v42
	v_dot4_i32_i8 v103, v96, v65, v103
	v_dot4_i32_i8 v104, v100, v69, v104
	v_and_b32_e32 v98, 0xf0f0f0f, v43
	v_and_b32_e32 v102, 0xf0f0f0f0, v43
	v_dot4_i32_i8 v103, v97, v66, v103
	v_dot4_i32_i8 v104, v101, v70, v104
	v_dot4_i32_i8 v103, v98, v67, v103
	v_dot4_i32_i8 v104, v102, v71, v104
	v_and_b32_e32 v95, 0xf0f0f0f, v44
	v_and_b32_e32 v99, 0xf0f0f0f0, v44
	v_and_b32_e32 v96, 0xf0f0f0f, v45
	v_and_b32_e32 v100, 0xf0f0f0f0, v45
	v_lshl_add_u32 v105, v103, 4, v104
	v_lshl_add_u32 v93, v105, 1, v72
	v_dot4_i32_i8 v126, v95, v64, 0
	v_dot4_i32_i8 v127, v99, v68, 0
	v_and_b32_e32 v97, 0xf0f0f0f, v46
	v_and_b32_e32 v101, 0xf0f0f0f0, v46
	v_dot4_i32_i8 v126, v96, v65, v126
	v_dot4_i32_i8 v127, v100, v69, v127
	v_and_b32_e32 v98, 0xf0f0f0f, v47
	v_and_b32_e32 v102, 0xf0f0f0f0, v47
	v_dot4_i32_i8 v126, v97, v66, v126
	v_dot4_i32_i8 v127, v101, v70, v127
	v_dot4_i32_i8 v126, v98, v67, v126
	v_dot4_i32_i8 v127, v102, v71, v127
	v_readlane_b32 s36, v75, 36
	v_readlane_b32 s5, v75, 37
	v_readlane_b32 s6, v75, 38
	v_lshl_add_u32 v105, v126, 4, v127
	v_lshl_add_u32 v94, v105, 1, v72
	v_cndmask_b32_e64 v107, v92, v91, s[38:39]
	v_cndmask_b32_e64 v109, v94, v93, s[38:39]
	v_cndmask_b32_e64 v106, v91, v92, s[38:39]
	v_cndmask_b32_e64 v108, v93, v94, s[38:39]
	v_add_u32_dpp v106, v107, v106 quad_perm:[1,0,3,2] row_mask:0xf bank_mask:0xf
	v_add_u32_dpp v108, v109, v108 quad_perm:[1,0,3,2] row_mask:0xf bank_mask:0xf
	v_readlane_b32 s7, v75, 39
	v_cndmask_b32_e64 v111, v108, v106, s[42:43]
	v_cndmask_b32_e64 v110, v106, v108, s[42:43]
	v_add_u32_e32 v113, s36, v206
	v_add_u32_e32 v114, s5, v206
	v_add_u32_dpp v110, v111, v110 quad_perm:[2,3,0,1] row_mask:0xf bank_mask:0xf
	v_add_u32_e32 v115, s6, v206
	v_add_u32_e32 v116, s7, v206
	v_add_u32_dpp v110, v110, v110 row_ror:4 row_mask:0xf bank_mask:0xf
	global_load_dwordx4 v[16:19], v113, s[52:53]
	global_load_dwordx4 v[20:23], v114, s[52:53]
	v_add_u32_dpp v110, v110, v110 row_ror:8 row_mask:0xf bank_mask:0xf
	global_load_dwordx4 v[24:27], v115, s[52:53]
	global_load_dwordx4 v[28:31], v116, s[52:53]
	s_lshl_b64 exec, s[22:23], 8
	v_mov_b32_e32 v84, v110
	v_mov_b32_e32 v88, s10
	s_mov_b64 exec, -1
.Lq_g7:
	s_add_u32 s11, s34, 28
	s_cmp_ge_u32 s11, s28
	s_cbranch_scc1 .Lq_end
	s_cmp_gt_u32 s50, 31
	s_cbranch_scc1 .Lq_stdg7
	s_add_u32 s36, s11, 20
	v_readlane_b32 s4, v81, s50
	s_cmp_lt_u32 s4, s36
	s_cbranch_scc1 .Lq_stxg7

; #define LAS __attribute__((address_space(3)))
; __device__ __forceinline__ int wave_isum4_t(const int (&d)[4], int lane) {
;     const bool o1 = lane & 1, o2 = lane & 2;
;     int a = o1 ? d[1] : d[0], b = o1 ? d[0] : d[1], c = o1 ? d[3] : d[2], e = o1 ? d[2] : d[3];
;     a += __builtin_amdgcn_update_dpp(0, b, 0xB1, 0xf, 0xf, true);
;     c += __builtin_amdgcn_update_dpp(0, e, 0xB1, 0xf, 0xf, true);
;     int f = o2 ? c : a, g = o2 ? a : c;
;     f += __builtin_amdgcn_update_dpp(0, g, 0x4E, 0xf, 0xf, true);
;     f += __builtin_amdgcn_update_dpp(0, f, 0x124, 0xf, 0xf, true);
;     f += __builtin_amdgcn_update_dpp(0, f, 0x128, 0xf, 0xf, true);
; __device__ __forceinline__ void peer3_dots(const u4 (&R)[PG][2], const u4 (&xq)[2], int sx15, LAS int* redrow, int g) {
;     ...
;     for (int k = 0; k < 4; ++k) { int a = 0, ah = 0;
; #pragma unroll
;         for (int q = 0; q < 4; ++q) { const unsigned w = R[k][0][q];
;             a = __builtin_amdgcn_sdot4((int)(w & 0x0f0f0f0fu), (int)xq[0][q], a, false); ah = __builtin_amdgcn_sdot4((int)(w & 0xf0f0f0f0u), (int)xq[1][q], ah, false); }
;         d[k] = 32 * a + 2 * ah - sx15; }
;     u4 w; w.x = (unsigned)d[0]; w.y = (unsigned)d[1]; w.z = (unsigned)d[2]; w.w = (unsigned)d[3];
;     *(LAS u4*)(redrow + 4 * g) = w;
.Lq_finret7:
	v_and_b32_e32 v95, 0xf0f0f0f, v48
	v_and_b32_e32 v99, 0xf0f0f0f0, v48
	v_and_b32_e32 v96, 0xf0f0f0f, v49
	v_and_b32_e32 v100, 0xf0f0f0f0, v49
	v_dot4_i32_i8 v103, v95, v64, 0
	v_dot4_i32_i8 v104, v99, v68, 0
	v_and_b32_e32 v97, 0xf0f0f0f, v50
	v_and_b32_e32 v101, 0xf0f0f0f0, v50
	v_dot4_i32_i8 v103, v96, v65, v103
	v_dot4_i32_i8 v104, v100, v69, v104
	v_and_b32_e32 v98, 0xf0f0f0f, v51
	v_and_b32_e32 v102, 0xf0f0f0f0, v51
	v_dot4_i32_i8 v103, v97, v66, v103
	v_dot4_i32_i8 v104, v101, v70, v104
	v_dot4_i32_i8 v103, v98, v67, v103
	v_dot4_i32_i8 v104, v102, v71, v104
	v_and_b32_e32 v95, 0xf0f0f0f, v52
	v_and_b32_e32 v99, 0xf0f0f0f0, v52
	v_and_b32_e32 v96, 0xf0f0f0f, v53
	v_and_b32_e32 v100, 0xf0f0f0f0, v53
	v_lshl_add_u32 v105, v103, 4, v104
	v_lshl_add_u32 v91, v105, 1, v72
	v_dot4_i32_i8 v126, v95, v64, 0
	v_dot4_i32_i8 v127, v99, v68, 0
	v_and_b32_e32 v97, 0xf0f0f0f, v54
	v_and_b32_e32 v101, 0xf0f0f0f0, v54
	v_dot4_i32_i8 v126, v96, v65, v126
	v_dot4_i32_i8 v127, v100, v69, v127
	v_and_b32_e32 v98, 0xf0f0f0f, v55
	v_and_b32_e32 v102, 0xf0f0f0f0, v55
	v_dot4_i32_i8 v126, v97, v66, v126
	v_dot4_i32_i8 v127, v101, v70, v127
	v_dot4_i32_i8 v126, v98, v67, v126
	v_dot4_i32_i8 v127, v102, v71, v127
	v_and_b32_e32 v95, 0xf0f0f0f, v56
	v_and_b32_e32 v99, 0xf0f0f0f0, v56
	v_and_b32_e32 v96, 0xf0f0f0f, v57
	v_and_b32_e32 v100, 0xf0f0f0f0, v57
	v_lshl_add_u32 v105, v126, 4, v127
	v_lshl_add_u32 v92, v105, 1, v72
	v_dot4_i32_i8 v103, v95, v64, 0
	v_dot4_i32_i8 v104, v99, v68, 0
	v_and_b32_e32 v97, 0xf0f0f0f, v58
	v_and_b32_e32 v101, 0xf0f0f0f0, v58
	v_dot4_i32_i8 v103, v96, v65, v103
	v_dot4_i32_i8 v104, v100, v69, v104
	v_and_b32_e32 v98, 0xf0f0f0f, v59
	v_and_b32_e32 v102, 0xf0f0f0f0, v59
	v_dot4_i32_i8 v103, v97, v66, v103
	v_dot4_i32_i8 v104, v101, v70, v104
	v_dot4_i32_i8 v103, v98, v67, v103
	v_dot4_i32_i8 v104, v102, v71, v104
	v_and_b32_e32 v95, 0xf0f0f0f, v60
	v_and_b32_e32 v99, 0xf0f0f0f0, v60
	v_and_b32_e32 v96, 0xf0f0f0f, v61
	v_and_b32_e32 v100, 0xf0f0f0f0, v61
	v_lshl_add_u32 v105, v103, 4, v104
	v_lshl_add_u32 v93, v105, 1, v72
	v_dot4_i32_i8 v126, v95, v64, 0
	v_dot4_i32_i8 v127, v99, v68, 0
	v_and_b32_e32 v97, 0xf0f0f0f, v62
	v_and_b32_e32 v101, 0xf0f0f0f0, v62
	v_dot4_i32_i8 v126, v96, v65, v126
	v_dot4_i32_i8 v127, v100, v69, v127
	v_and_b32_e32 v98, 0xf0f0f0f, v63
	v_and_b32_e32 v102, 0xf0f0f0f0, v63
	v_dot4_i32_i8 v126, v97, v66, v126
	v_dot4_i32_i8 v127, v101, v70, v127
	v_dot4_i32_i8 v126, v98, v67, v126
	v_dot4_i32_i8 v127, v102, v71, v127
	v_readlane_b32 s36, v75, 40
	v_readlane_b32 s5, v75, 41
	v_readlane_b32 s6, v75, 42
	v_lshl_add_u32 v105, v126, 4, v127
	v_lshl_add_u32 v94, v105, 1, v72
	v_cndmask_b32_e64 v107, v92, v91, s[38:39]
	v_cndmask_b32_e64 v109, v94, v93, s[38:39]
	v_cndmask_b32_e64 v106, v91, v92, s[38:39]
	v_cndmask_b32_e64 v108, v93, v94, s[38:39]
	v_add_u32_dpp v106, v107, v106 quad_perm:[1,0,3,2] row_mask:0xf bank_mask:0xf
	v_add_u32_dpp v108, v109, v108 quad_perm:[1,0,3,2] row_mask:0xf bank_mask:0xf
	v_readlane_b32 s7, v75, 43
	v_cndmask_b32_e64 v111, v108, v106, s[42:43]
	v_cndmask_b32_e64 v110, v106, v108, s[42:43]
	v_add_u32_e32 v113, s36, v206
	v_add_u32_e32 v114, s5, v206
	v_add_u32_dpp v110, v111, v110 quad_perm:[2,3,0,1] row_mask:0xf bank_mask:0xf
	v_add_u32_e32 v115, s6, v206
	v_add_u32_e32 v116, s7, v206
	v_add_u32_dpp v110, v110, v110 row_ror:4 row_mask:0xf bank_mask:0xf
	global_load_dwordx4 v[32:35], v113, s[52:53]
	global_load_dwordx4 v[36:39], v114, s[52:53]
	v_add_u32_dpp v110, v110, v110 row_ror:8 row_mask:0xf bank_mask:0xf
	global_load_dwordx4 v[40:43], v115, s[52:53]
	global_load_dwordx4 v[44:47], v116, s[52:53]
	s_lshl_b64 exec, s[22:23], 12
	v_mov_b32_e32 v84, v110
	v_mov_b32_e32 v88, s10
	s_mov_b64 exec, -1
.Lq_g8:
	s_add_u32 s11, s34, 32
	s_cmp_ge_u32 s11, s28
	s_cbranch_scc1 .Lq_end
	s_cmp_gt_u32 s50, 31
	s_cbranch_scc1 .Lq_stdg8
	s_add_u32 s36, s11, 20
	v_readlane_b32 s4, v81, s50
	s_cmp_lt_u32 s4, s36
	s_cbranch_scc1 .Lq_stxg8

; #define LAS __attribute__((address_space(3)))
; __device__ __forceinline__ int wave_isum4_t(const int (&d)[4], int lane) {
;     const bool o1 = lane & 1, o2 = lane & 2;
;     int a = o1 ? d[1] : d[0], b = o1 ? d[0] : d[1], c = o1 ? d[3] : d[2], e = o1 ? d[2] : d[3];
;     a += __builtin_amdgcn_update_dpp(0, b, 0xB1, 0xf, 0xf, true);
;     c += __builtin_amdgcn_update_dpp(0, e, 0xB1, 0xf, 0xf, true);
;     int f = o2 ? c : a, g = o2 ? a : c;
;     f += __builtin_amdgcn_update_dpp(0, g, 0x4E, 0xf, 0xf, true);
;     f += __builtin_amdgcn_update_dpp(0, f, 0x124, 0xf, 0xf, true);
;     f += __builtin_amdgcn_update_dpp(0, f, 0x128, 0xf, 0xf, true);
; __device__ __forceinline__ void peer3_dots(const u4 (&R)[PG][2], const u4 (&xq)[2], int sx15, LAS int* redrow, int g) {
;     ...
;     for (int k = 0; k < 4; ++k) { int a = 0, ah = 0;
; #pragma unroll
;         for (int q = 0; q < 4; ++q) { const unsigned w = R[k][0][q];
;             a = __builtin_amdgcn_sdot4((int)(w & 0x0f0f0f0fu), (int)xq[0][q], a, false); ah = __builtin_amdgcn_sdot4((int)(w & 0xf0f0f0f0u), (int)xq[1][q], ah, false); }
;         d[k] = 32 * a + 2 * ah - sx15; }
;     u4 w; w.x = (unsigned)d[0]; w.y = (unsigned)d[1]; w.z = (unsigned)d[2]; w.w = (unsigned)d[3];
;     *(LAS u4*)(redrow + 4 * g) = w;
.Lq_finret8:
	v_and_b32_e32 v95, 0xf0f0f0f, v0
	v_and_b32_e32 v99, 0xf0f0f0f0, v0
	v_and_b32_e32 v96, 0xf0f0f0f, v1
	v_and_b32_e32 v100, 0xf0f0f0f0, v1
	v_dot4_i32_i8 v103, v95, v64, 0
	v_dot4_i32_i8 v104, v99, v68, 0
	v_and_b32_e32 v97, 0xf0f0f0f, v2
	v_and_b32_e32 v101, 0xf0f0f0f0, v2
	v_dot4_i32_i8 v103, v96, v65, v103
	v_dot4_i32_i8 v104, v100, v69, v104
	v_and_b32_e32 v98, 0xf0f0f0f, v3
	v_and_b32_e32 v102, 0xf0f0f0f0, v3
	v_dot4_i32_i8 v103, v97, v66, v103
	v_dot4_i32_i8 v104, v101, v70, v104
	v_dot4_i32_i8 v103, v98, v67, v103
	v_dot4_i32_i8 v104, v102, v71, v104
	v_and_b32_e32 v95, 0xf0f0f0f, v4
	v_and_b32_e32 v99, 0xf0f0f0f0, v4
	v_and_b32_e32 v96, 0xf0f0f0f, v5
	v_and_b32_e32 v100, 0xf0f0f0f0, v5
	v_lshl_add_u32 v105, v103, 4, v104
	v_lshl_add_u32 v91, v105, 1, v72
	v_dot4_i32_i8 v126, v95, v64, 0
	v_dot4_i32_i8 v127, v99, v68, 0
	v_and_b32_e32 v97, 0xf0f0f0f, v6
	v_and_b32_e32 v101, 0xf0f0f0f0, v6
	v_dot4_i32_i8 v126, v96, v65, v126
	v_dot4_i32_i8 v127, v100, v69, v127
	v_and_b32_e32 v98, 0xf0f0f0f, v7
	v_and_b32_e32 v102, 0xf0f0f0f0, v7
	v_dot4_i32_i8 v126, v97, v66, v126
	v_dot4_i32_i8 v127, v101, v70, v127
	v_dot4_i32_i8 v126, v98, v67, v126
	v_dot4_i32_i8 v127, v102, v71, v127
	v_and_b32_e32 v95, 0xf0f0f0f, v8
	v_and_b32_e32 v99, 0xf0f0f0f0, v8
	v_and_b32_e32 v96, 0xf0f0f0f, v9
	v_and_b32_e32 v100, 0xf0f0f0f0, v9
	v_lshl_add_u32 v105, v126, 4, v127
	v_lshl_add_u32 v92, v105, 1, v72
	v_dot4_i32_i8 v103, v95, v64, 0
	v_dot4_i32_i8 v104, v99, v68, 0
	v_and_b32_e32 v97, 0xf0f0f0f, v10
	v_and_b32_e32 v101, 0xf0f0f0f0, v10
	v_dot4_i32_i8 v103, v96, v65, v103
	v_dot4_i32_i8 v104, v100, v69, v104
	v_and_b32_e32 v98, 0xf0f0f0f, v11
	v_and_b32_e32 v102, 0xf0f0f0f0, v11
	v_dot4_i32_i8 v103, v97, v66, v103
	v_dot4_i32_i8 v104, v101, v70, v104
	v_dot4_i32_i8 v103, v98, v67, v103
	v_dot4_i32_i8 v104, v102, v71, v104
	v_and_b32_e32 v95, 0xf0f0f0f, v12
	v_and_b32_e32 v99, 0xf0f0f0f0, v12
	v_and_b32_e32 v96, 0xf0f0f0f, v13
	v_and_b32_e32 v100, 0xf0f0f0f0, v13
	v_lshl_add_u32 v105, v103, 4, v104
	v_lshl_add_u32 v93, v105, 1, v72
	v_dot4_i32_i8 v126, v95, v64, 0
	v_dot4_i32_i8 v127, v99, v68, 0
	v_and_b32_e32 v97, 0xf0f0f0f, v14
	v_and_b32_e32 v101, 0xf0f0f0f0, v14
	v_dot4_i32_i8 v126, v96, v65, v126
	v_dot4_i32_i8 v127, v100, v69, v127
	v_and_b32_e32 v98, 0xf0f0f0f, v15
	v_and_b32_e32 v102, 0xf0f0f0f0, v15
	v_dot4_i32_i8 v126, v97, v66, v126
	v_dot4_i32_i8 v127, v101, v70, v127
	v_dot4_i32_i8 v126, v98, v67, v126
	v_dot4_i32_i8 v127, v102, v71, v127
	v_readlane_b32 s36, v75, 44
	v_readlane_b32 s5, v75, 45
	v_readlane_b32 s6, v75, 46
	v_lshl_add_u32 v105, v126, 4, v127
	v_lshl_add_u32 v94, v105, 1, v72
	v_cndmask_b32_e64 v107, v92, v91, s[38:39]
	v_cndmask_b32_e64 v109, v94, v93, s[38:39]
	v_cndmask_b32_e64 v106, v91, v92, s[38:39]
	v_cndmask_b32_e64 v108, v93, v94, s[38:39]
	v_add_u32_dpp v106, v107, v106 quad_perm:[1,0,3,2] row_mask:0xf bank_mask:0xf
	v_add_u32_dpp v108, v109, v108 quad_perm:[1,0,3,2] row_mask:0xf bank_mask:0xf
	v_readlane_b32 s7, v75, 47
	v_cndmask_b32_e64 v111, v108, v106, s[42:43]
	v_cndmask_b32_e64 v110, v106, v108, s[42:43]
	v_add_u32_e32 v113, s36, v206
	v_add_u32_e32 v114, s5, v206
	v_add_u32_dpp v110, v111, v110 quad_perm:[2,3,0,1] row_mask:0xf bank_mask:0xf
	v_add_u32_e32 v115, s6, v206
	v_add_u32_e32 v116, s7, v206
	v_add_u32_dpp v110, v110, v110 row_ror:4 row_mask:0xf bank_mask:0xf
	global_load_dwordx4 v[48:51], v113, s[52:53]
	global_load_dwordx4 v[52:55], v114, s[52:53]
	v_add_u32_dpp v110, v110, v110 row_ror:8 row_mask:0xf bank_mask:0xf
	global_load_dwordx4 v[56:59], v115, s[52:53]
	global_load_dwordx4 v[60:63], v116, s[52:53]
	s_mov_b64 exec, s[22:23]
	v_mov_b32_e32 v85, v110
	v_mov_b32_e32 v89, s10
	s_mov_b64 exec, -1
.Lq_g9:
	s_add_u32 s11, s34, 36
	s_cmp_ge_u32 s11, s28
	s_cbranch_scc1 .Lq_end
	s_cmp_gt_u32 s50, 31
	s_cbranch_scc1 .Lq_stdg9
	s_add_u32 s36, s11, 20
	v_readlane_b32 s4, v81, s50
	s_cmp_lt_u32 s4, s36
	s_cbranch_scc1 .Lq_stxg9

; #define LAS __attribute__((address_space(3)))
; __device__ __forceinline__ int wave_isum4_t(const int (&d)[4], int lane) {
;     const bool o1 = lane & 1, o2 = lane & 2;
;     int a = o1 ? d[1] : d[0], b = o1 ? d[0] : d[1], c = o1 ? d[3] : d[2], e = o1 ? d[2] : d[3];
;     a += __builtin_amdgcn_update_dpp(0, b, 0xB1, 0xf, 0xf, true);
;     c += __builtin_amdgcn_update_dpp(0, e, 0xB1, 0xf, 0xf, true);
;     int f = o2 ? c : a, g = o2 ? a : c;
;     f += __builtin_amdgcn_update_dpp(0, g, 0x4E, 0xf, 0xf, true);
;     f += __builtin_amdgcn_update_dpp(0, f, 0x124, 0xf, 0xf, true);
;     f += __builtin_amdgcn_update_dpp(0, f, 0x128, 0xf, 0xf, true);
; __device__ __forceinline__ void peer3_dots(const u4 (&R)[PG][2], const u4 (&xq)[2], int sx15, LAS int* redrow, int g) {
;     ...
;     for (int k = 0; k < 4; ++k) { int a = 0, ah = 0;
; #pragma unroll
;         for (int q = 0; q < 4; ++q) { const unsigned w = R[k][0][q];
;             a = __builtin_amdgcn_sdot4((int)(w & 0x0f0f0f0fu), (int)xq[0][q], a, false); ah = __builtin_amdgcn_sdot4((int)(w & 0xf0f0f0f0u), (int)xq[1][q], ah, false); }
;         d[k] = 32 * a + 2 * ah - sx15; }
;     u4 w; w.x = (unsigned)d[0]; w.y = (unsigned)d[1]; w.z = (unsigned)d[2]; w.w = (unsigned)d[3];
;     *(LAS u4*)(redrow + 4 * g) = w;
.Lq_finret9:
	v_and_b32_e32 v95, 0xf0f0f0f, v16
	v_and_b32_e32 v99, 0xf0f0f0f0, v16
	v_and_b32_e32 v96, 0xf0f0f0f, v17
	v_and_b32_e32 v100, 0xf0f0f0f0, v17
	v_dot4_i32_i8 v103, v95, v64, 0
	v_dot4_i32_i8 v104, v99, v68, 0
	v_and_b32_e32 v97, 0xf0f0f0f, v18
	v_and_b32_e32 v101, 0xf0f0f0f0, v18
	v_dot4_i32_i8 v103, v96, v65, v103
	v_dot4_i32_i8 v104, v100, v69, v104
	v_and_b32_e32 v98, 0xf0f0f0f, v19
	v_and_b32_e32 v102, 0xf0f0f0f0, v19
	v_dot4_i32_i8 v103, v97, v66, v103
	v_dot4_i32_i8 v104, v101, v70, v104
	v_dot4_i32_i8 v103, v98, v67, v103
	v_dot4_i32_i8 v104, v102, v71, v104
	v_and_b32_e32 v95, 0xf0f0f0f, v20
	v_and_b32_e32 v99, 0xf0f0f0f0, v20
	v_and_b32_e32 v96, 0xf0f0f0f, v21
	v_and_b32_e32 v100, 0xf0f0f0f0, v21
	v_lshl_add_u32 v105, v103, 4, v104
	v_lshl_add_u32 v91, v105, 1, v72
	v_dot4_i32_i8 v126, v95, v64, 0
	v_dot4_i32_i8 v127, v99, v68, 0
	v_and_b32_e32 v97, 0xf0f0f0f, v22
	v_and_b32_e32 v101, 0xf0f0f0f0, v22
	v_dot4_i32_i8 v126, v96, v65, v126
	v_dot4_i32_i8 v127, v100, v69, v127
	v_and_b32_e32 v98, 0xf0f0f0f, v23
	v_and_b32_e32 v102, 0xf0f0f0f0, v23
	v_dot4_i32_i8 v126, v97, v66, v126
	v_dot4_i32_i8 v127, v101, v70, v127
	v_dot4_i32_i8 v126, v98, v67, v126
	v_dot4_i32_i8 v127, v102, v71, v127
	v_and_b32_e32 v95, 0xf0f0f0f, v24
	v_and_b32_e32 v99, 0xf0f0f0f0, v24
	v_and_b32_e32 v96, 0xf0f0f0f, v25
	v_and_b32_e32 v100, 0xf0f0f0f0, v25
	v_lshl_add_u32 v105, v126, 4, v127
	v_lshl_add_u32 v92, v105, 1, v72
	v_dot4_i32_i8 v103, v95, v64, 0
	v_dot4_i32_i8 v104, v99, v68, 0
	v_and_b32_e32 v97, 0xf0f0f0f, v26
	v_and_b32_e32 v101, 0xf0f0f0f0, v26
	v_dot4_i32_i8 v103, v96, v65, v103
	v_dot4_i32_i8 v104, v100, v69, v104
	v_and_b32_e32 v98, 0xf0f0f0f, v27
	v_and_b32_e32 v102, 0xf0f0f0f0, v27
	v_dot4_i32_i8 v103, v97, v66, v103
	v_dot4_i32_i8 v104, v101, v70, v104
	v_dot4_i32_i8 v103, v98, v67, v103
	v_dot4_i32_i8 v104, v102, v71, v104
	v_and_b32_e32 v95, 0xf0f0f0f, v28
	v_and_b32_e32 v99, 0xf0f0f0f0, v28
	v_and_b32_e32 v96, 0xf0f0f0f, v29
	v_and_b32_e32 v100, 0xf0f0f0f0, v29
	v_lshl_add_u32 v105, v103, 4, v104
	v_lshl_add_u32 v93, v105, 1, v72
	v_dot4_i32_i8 v126, v95, v64, 0
	v_dot4_i32_i8 v127, v99, v68, 0
	v_and_b32_e32 v97, 0xf0f0f0f, v30
	v_and_b32_e32 v101, 0xf0f0f0f0, v30
	v_dot4_i32_i8 v126, v96, v65, v126
	v_dot4_i32_i8 v127, v100, v69, v127
	v_and_b32_e32 v98, 0xf0f0f0f, v31
	v_and_b32_e32 v102, 0xf0f0f0f0, v31
	v_dot4_i32_i8 v126, v97, v66, v126
	v_dot4_i32_i8 v127, v101, v70, v127
	v_dot4_i32_i8 v126, v98, v67, v126
	v_dot4_i32_i8 v127, v102, v71, v127
	v_readlane_b32 s36, v75, 48
	v_readlane_b32 s5, v75, 49
	v_readlane_b32 s6, v75, 50
	v_lshl_add_u32 v105, v126, 4, v127
	v_lshl_add_u32 v94, v105, 1, v72
	v_cndmask_b32_e64 v107, v92, v91, s[38:39]
	v_cndmask_b32_e64 v109, v94, v93, s[38:39]
	v_cndmask_b32_e64 v106, v91, v92, s[38:39]
	v_cndmask_b32_e64 v108, v93, v94, s[38:39]
	v_add_u32_dpp v106, v107, v106 quad_perm:[1,0,3,2] row_mask:0xf bank_mask:0xf
	v_add_u32_dpp v108, v109, v108 quad_perm:[1,0,3,2] row_mask:0xf bank_mask:0xf
	v_readlane_b32 s7, v75, 51
	v_cndmask_b32_e64 v111, v108, v106, s[42:43]
	v_cndmask_b32_e64 v110, v106, v108, s[42:43]
	v_add_u32_e32 v113, s36, v206
	v_add_u32_e32 v114, s5, v206
	v_add_u32_dpp v110, v111, v110 quad_perm:[2,3,0,1] row_mask:0xf bank_mask:0xf
	v_add_u32_e32 v115, s6, v206
	v_add_u32_e32 v116, s7, v206
	v_add_u32_dpp v110, v110, v110 row_ror:4 row_mask:0xf bank_mask:0xf
	global_load_dwordx4 v[0:3], v113, s[52:53]
	global_load_dwordx4 v[4:7], v114, s[52:53]
	v_add_u32_dpp v110, v110, v110 row_ror:8 row_mask:0xf bank_mask:0xf
	global_load_dwordx4 v[8:11], v115, s[52:53]
	global_load_dwordx4 v[12:15], v116, s[52:53]
	s_lshl_b64 exec, s[22:23], 4
	v_mov_b32_e32 v85, v110
	v_mov_b32_e32 v89, s10
	s_mov_b64 exec, -1
.Lq_g10:
	s_add_u32 s11, s34, 40
	s_cmp_ge_u32 s11, s28
	s_cbranch_scc1 .Lq_end
	s_cmp_gt_u32 s50, 31
	s_cbranch_scc1 .Lq_stdg10
	s_add_u32 s36, s11, 20
	v_readlane_b32 s4, v81, s50
	s_cmp_lt_u32 s4, s36
	s_cbranch_scc1 .Lq_stxg10

; #define LAS __attribute__((address_space(3)))
; __device__ __forceinline__ int wave_isum4_t(const int (&d)[4], int lane) {
;     const bool o1 = lane & 1, o2 = lane & 2;
;     int a = o1 ? d[1] : d[0], b = o1 ? d[0] : d[1], c = o1 ? d[3] : d[2], e = o1 ? d[2] : d[3];
;     a += __builtin_amdgcn_update_dpp(0, b, 0xB1, 0xf, 0xf, true);
;     c += __builtin_amdgcn_update_dpp(0, e, 0xB1, 0xf, 0xf, true);
;     int f = o2 ? c : a, g = o2 ? a : c;
;     f += __builtin_amdgcn_update_dpp(0, g, 0x4E, 0xf, 0xf, true);
;     f += __builtin_amdgcn_update_dpp(0, f, 0x124, 0xf, 0xf, true);
;     f += __builtin_amdgcn_update_dpp(0, f, 0x128, 0xf, 0xf, true);
; __device__ __forceinline__ void peer3_dots(const u4 (&R)[PG][2], const u4 (&xq)[2], int sx15, LAS int* redrow, int g) {
;     ...
;     for (int k = 0; k < 4; ++k) { int a = 0, ah = 0;
; #pragma unroll
;         for (int q = 0; q < 4; ++q) { const unsigned w = R[k][0][q];
;             a = __builtin_amdgcn_sdot4((int)(w & 0x0f0f0f0fu), (int)xq[0][q], a, false); ah = __builtin_amdgcn_sdot4((int)(w & 0xf0f0f0f0u), (int)xq[1][q], ah, false); }
;         d[k] = 32 * a + 2 * ah - sx15; }
;     u4 w; w.x = (unsigned)d[0]; w.y = (unsigned)d[1]; w.z = (unsigned)d[2]; w.w = (unsigned)d[3];
;     *(LAS u4*)(redrow + 4 * g) = w;
.Lq_finret10:
	v_and_b32_e32 v95, 0xf0f0f0f, v32
	v_and_b32_e32 v99, 0xf0f0f0f0, v32
	v_and_b32_e32 v96, 0xf0f0f0f, v33
	v_and_b32_e32 v100, 0xf0f0f0f0, v33
	v_dot4_i32_i8 v103, v95, v64, 0
	v_dot4_i32_i8 v104, v99, v68, 0
	v_and_b32_e32 v97, 0xf0f0f0f, v34
	v_and_b32_e32 v101, 0xf0f0f0f0, v34
	v_dot4_i32_i8 v103, v96, v65, v103
	v_dot4_i32_i8 v104, v100, v69, v104
	v_and_b32_e32 v98, 0xf0f0f0f, v35
	v_and_b32_e32 v102, 0xf0f0f0f0, v35
	v_dot4_i32_i8 v103, v97, v66, v103
	v_dot4_i32_i8 v104, v101, v70, v104
	v_dot4_i32_i8 v103, v98, v67, v103
	v_dot4_i32_i8 v104, v102, v71, v104
	v_and_b32_e32 v95, 0xf0f0f0f, v36
	v_and_b32_e32 v99, 0xf0f0f0f0, v36
	v_and_b32_e32 v96, 0xf0f0f0f, v37
	v_and_b32_e32 v100, 0xf0f0f0f0, v37
	v_lshl_add_u32 v105, v103, 4, v104
	v_lshl_add_u32 v91, v105, 1, v72
	v_dot4_i32_i8 v126, v95, v64, 0
	v_dot4_i32_i8 v127, v99, v68, 0
	v_and_b32_e32 v97, 0xf0f0f0f, v38
	v_and_b32_e32 v101, 0xf0f0f0f0, v38
	v_dot4_i32_i8 v126, v96, v65, v126
	v_dot4_i32_i8 v127, v100, v69, v127
	v_and_b32_e32 v98, 0xf0f0f0f, v39
	v_and_b32_e32 v102, 0xf0f0f0f0, v39
	v_dot4_i32_i8 v126, v97, v66, v126
	v_dot4_i32_i8 v127, v101, v70, v127
	v_dot4_i32_i8 v126, v98, v67, v126
	v_dot4_i32_i8 v127, v102, v71, v127
	v_and_b32_e32 v95, 0xf0f0f0f, v40
	v_and_b32_e32 v99, 0xf0f0f0f0, v40
	v_and_b32_e32 v96, 0xf0f0f0f, v41
	v_and_b32_e32 v100, 0xf0f0f0f0, v41
	v_lshl_add_u32 v105, v126, 4, v127
	v_lshl_add_u32 v92, v105, 1, v72
	v_dot4_i32_i8 v103, v95, v64, 0
	v_dot4_i32_i8 v104, v99, v68, 0
	v_and_b32_e32 v97, 0xf0f0f0f, v42
	v_and_b32_e32 v101, 0xf0f0f0f0, v42
	v_dot4_i32_i8 v103, v96, v65, v103
	v_dot4_i32_i8 v104, v100, v69, v104
	v_and_b32_e32 v98, 0xf0f0f0f, v43
	v_and_b32_e32 v102, 0xf0f0f0f0, v43
	v_dot4_i32_i8 v103, v97, v66, v103
	v_dot4_i32_i8 v104, v101, v70, v104
	v_dot4_i32_i8 v103, v98, v67, v103
	v_dot4_i32_i8 v104, v102, v71, v104
	v_and_b32_e32 v95, 0xf0f0f0f, v44
	v_and_b32_e32 v99, 0xf0f0f0f0, v44
	v_and_b32_e32 v96, 0xf0f0f0f, v45
	v_and_b32_e32 v100, 0xf0f0f0f0, v45
	v_lshl_add_u32 v105, v103, 4, v104
	v_lshl_add_u32 v93, v105, 1, v72
	v_dot4_i32_i8 v126, v95, v64, 0
	v_dot4_i32_i8 v127, v99, v68, 0
	v_and_b32_e32 v97, 0xf0f0f0f, v46
	v_and_b32_e32 v101, 0xf0f0f0f0, v46
	v_dot4_i32_i8 v126, v96, v65, v126
	v_dot4_i32_i8 v127, v100, v69, v127
	v_and_b32_e32 v98, 0xf0f0f0f, v47
	v_and_b32_e32 v102, 0xf0f0f0f0, v47
	v_dot4_i32_i8 v126, v97, v66, v126
	v_dot4_i32_i8 v127, v101, v70, v127
	v_dot4_i32_i8 v126, v98, v67, v126
	v_dot4_i32_i8 v127, v102, v71, v127
	v_readlane_b32 s36, v75, 52
	v_readlane_b32 s5, v75, 53
	v_readlane_b32 s6, v75, 54
	v_lshl_add_u32 v105, v126, 4, v127
	v_lshl_add_u32 v94, v105, 1, v72
	v_cndmask_b32_e64 v107, v92, v91, s[38:39]
	v_cndmask_b32_e64 v109, v94, v93, s[38:39]
	v_cndmask_b32_e64 v106, v91, v92, s[38:39]
	v_cndmask_b32_e64 v108, v93, v94, s[38:39]
	v_add_u32_dpp v106, v107, v106 quad_perm:[1,0,3,2] row_mask:0xf bank_mask:0xf
	v_add_u32_dpp v108, v109, v108 quad_perm:[1,0,3,2] row_mask:0xf bank_mask:0xf
	v_readlane_b32 s7, v75, 55
	v_cndmask_b32_e64 v111, v108, v106, s[42:43]
	v_cndmask_b32_e64 v110, v106, v108, s[42:43]
	v_add_u32_e32 v113, s36, v206
	v_add_u32_e32 v114, s5, v206
	v_add_u32_dpp v110, v111, v110 quad_perm:[2,3,0,1] row_mask:0xf bank_mask:0xf
	v_add_u32_e32 v115, s6, v206
	v_add_u32_e32 v116, s7, v206
	v_add_u32_dpp v110, v110, v110 row_ror:4 row_mask:0xf bank_mask:0xf
	global_load_dwordx4 v[16:19], v113, s[52:53]
	global_load_dwordx4 v[20:23], v114, s[52:53]
	v_add_u32_dpp v110, v110, v110 row_ror:8 row_mask:0xf bank_mask:0xf
	global_load_dwordx4 v[24:27], v115, s[52:53]
	global_load_dwordx4 v[28:31], v116, s[52:53]
	s_lshl_b64 exec, s[22:23], 8
	v_mov_b32_e32 v85, v110
	v_mov_b32_e32 v89, s10
	s_mov_b64 exec, -1
.Lq_g11:
	s_add_u32 s11, s34, 44
	s_cmp_ge_u32 s11, s28
	s_cbranch_scc1 .Lq_end
	s_cmp_gt_u32 s50, 31
	s_cbranch_scc1 .Lq_stdg11
	s_add_u32 s36, s11, 20
	v_readlane_b32 s4, v81, s50
	s_cmp_lt_u32 s4, s36
	s_cbranch_scc1 .Lq_stxg11

; #define LAS __attribute__((address_space(3)))
; __device__ __forceinline__ int wave_isum4_t(const int (&d)[4], int lane) {
;     const bool o1 = lane & 1, o2 = lane & 2;
;     int a = o1 ? d[1] : d[0], b = o1 ? d[0] : d[1], c = o1 ? d[3] : d[2], e = o1 ? d[2] : d[3];
;     a += __builtin_amdgcn_update_dpp(0, b, 0xB1, 0xf, 0xf, true);
;     c += __builtin_amdgcn_update_dpp(0, e, 0xB1, 0xf, 0xf, true);
;     int f = o2 ? c : a, g = o2 ? a : c;
;     f += __builtin_amdgcn_update_dpp(0, g, 0x4E, 0xf, 0xf, true);
;     f += __builtin_amdgcn_update_dpp(0, f, 0x124, 0xf, 0xf, true);
;     f += __builtin_amdgcn_update_dpp(0, f, 0x128, 0xf, 0xf, true);
; __device__ __forceinline__ void peer3_dots(const u4 (&R)[PG][2], const u4 (&xq)[2], int sx15, LAS int* redrow, int g) {
;     ...
;     for (int k = 0; k < 4; ++k) { int a = 0, ah = 0;
; #pragma unroll
;         for (int q = 0; q < 4; ++q) { const unsigned w = R[k][0][q];
;             a = __builtin_amdgcn_sdot4((int)(w & 0x0f0f0f0fu), (int)xq[0][q], a, false); ah = __builtin_amdgcn_sdot4((int)(w & 0xf0f0f0f0u), (int)xq[1][q], ah, false); }
;         d[k] = 32 * a + 2 * ah - sx15; }
;     u4 w; w.x = (unsigned)d[0]; w.y = (unsigned)d[1]; w.z = (unsigned)d[2]; w.w = (unsigned)d[3];
;     *(LAS u4*)(redrow + 4 * g) = w;
.Lq_finret11:
	v_and_b32_e32 v95, 0xf0f0f0f, v48
	v_and_b32_e32 v99, 0xf0f0f0f0, v48
	v_and_b32_e32 v96, 0xf0f0f0f, v49
	v_and_b32_e32 v100, 0xf0f0f0f0, v49
	v_dot4_i32_i8 v103, v95, v64, 0
	v_dot4_i32_i8 v104, v99, v68, 0
	v_and_b32_e32 v97, 0xf0f0f0f, v50
	v_and_b32_e32 v101, 0xf0f0f0f0, v50
	v_dot4_i32_i8 v103, v96, v65, v103
	v_dot4_i32_i8 v104, v100, v69, v104
	v_and_b32_e32 v98, 0xf0f0f0f, v51
	v_and_b32_e32 v102, 0xf0f0f0f0, v51
	v_dot4_i32_i8 v103, v97, v66, v103
	v_dot4_i32_i8 v104, v101, v70, v104
	v_dot4_i32_i8 v103, v98, v67, v103
	v_dot4_i32_i8 v104, v102, v71, v104
	v_and_b32_e32 v95, 0xf0f0f0f, v52
	v_and_b32_e32 v99, 0xf0f0f0f0, v52
	v_and_b32_e32 v96, 0xf0f0f0f, v53
	v_and_b32_e32 v100, 0xf0f0f0f0, v53
	v_lshl_add_u32 v105, v103, 4, v104
	v_lshl_add_u32 v91, v105, 1, v72
	v_dot4_i32_i8 v126, v95, v64, 0
	v_dot4_i32_i8 v127, v99, v68, 0
	v_and_b32_e32 v97, 0xf0f0f0f, v54
	v_and_b32_e32 v101, 0xf0f0f0f0, v54
	v_dot4_i32_i8 v126, v96, v65, v126
	v_dot4_i32_i8 v127, v100, v69, v127
	v_and_b32_e32 v98, 0xf0f0f0f, v55
	v_and_b32_e32 v102, 0xf0f0f0f0, v55
	v_dot4_i32_i8 v126, v97, v66, v126
	v_dot4_i32_i8 v127, v101, v70, v127
	v_dot4_i32_i8 v126, v98, v67, v126
	v_dot4_i32_i8 v127, v102, v71, v127
	v_and_b32_e32 v95, 0xf0f0f0f, v56
	v_and_b32_e32 v99, 0xf0f0f0f0, v56
	v_and_b32_e32 v96, 0xf0f0f0f, v57
	v_and_b32_e32 v100, 0xf0f0f0f0, v57
	v_lshl_add_u32 v105, v126, 4, v127
	v_lshl_add_u32 v92, v105, 1, v72
	v_dot4_i32_i8 v103, v95, v64, 0
	v_dot4_i32_i8 v104, v99, v68, 0
	v_and_b32_e32 v97, 0xf0f0f0f, v58
	v_and_b32_e32 v101, 0xf0f0f0f0, v58
	v_dot4_i32_i8 v103, v96, v65, v103
	v_dot4_i32_i8 v104, v100, v69, v104
	v_and_b32_e32 v98, 0xf0f0f0f, v59
	v_and_b32_e32 v102, 0xf0f0f0f0, v59
	v_dot4_i32_i8 v103, v97, v66, v103
	v_dot4_i32_i8 v104, v101, v70, v104
	v_dot4_i32_i8 v103, v98, v67, v103
	v_dot4_i32_i8 v104, v102, v71, v104
	v_and_b32_e32 v95, 0xf0f0f0f, v60
	v_and_b32_e32 v99, 0xf0f0f0f0, v60
	v_and_b32_e32 v96, 0xf0f0f0f, v61
	v_and_b32_e32 v100, 0xf0f0f0f0, v61
	v_lshl_add_u32 v105, v103, 4, v104
	v_lshl_add_u32 v93, v105, 1, v72
	v_dot4_i32_i8 v126, v95, v64, 0
	v_dot4_i32_i8 v127, v99, v68, 0
	v_and_b32_e32 v97, 0xf0f0f0f, v62
	v_and_b32_e32 v101, 0xf0f0f0f0, v62
	v_dot4_i32_i8 v126, v96, v65, v126
	v_dot4_i32_i8 v127, v100, v69, v127
	v_and_b32_e32 v98, 0xf0f0f0f, v63
	v_and_b32_e32 v102, 0xf0f0f0f0, v63
	v_dot4_i32_i8 v126, v97, v66, v126
	v_dot4_i32_i8 v127, v101, v70, v127
	v_dot4_i32_i8 v126, v98, v67, v126
	v_dot4_i32_i8 v127, v102, v71, v127
	v_readlane_b32 s36, v75, 56
	v_readlane_b32 s5, v75, 57
	v_readlane_b32 s6, v75, 58
	v_lshl_add_u32 v105, v126, 4, v127
	v_lshl_add_u32 v94, v105, 1, v72
	v_cndmask_b32_e64 v107, v92, v91, s[38:39]
	v_cndmask_b32_e64 v109, v94, v93, s[38:39]
	v_cndmask_b32_e64 v106, v91, v92, s[38:39]
	v_cndmask_b32_e64 v108, v93, v94, s[38:39]
	v_add_u32_dpp v106, v107, v106 quad_perm:[1,0,3,2] row_mask:0xf bank_mask:0xf
	v_add_u32_dpp v108, v109, v108 quad_perm:[1,0,3,2] row_mask:0xf bank_mask:0xf
	v_readlane_b32 s7, v75, 59
	v_cndmask_b32_e64 v111, v108, v106, s[42:43]
	v_cndmask_b32_e64 v110, v106, v108, s[42:43]
	v_add_u32_e32 v113, s36, v206
	v_add_u32_e32 v114, s5, v206
	v_add_u32_dpp v110, v111, v110 quad_perm:[2,3,0,1] row_mask:0xf bank_mask:0xf
	v_add_u32_e32 v115, s6, v206
	v_add_u32_e32 v116, s7, v206
	v_add_u32_dpp v110, v110, v110 row_ror:4 row_mask:0xf bank_mask:0xf
	global_load_dwordx4 v[32:35], v113, s[52:53]
	global_load_dwordx4 v[36:39], v114, s[52:53]
	v_add_u32_dpp v110, v110, v110 row_ror:8 row_mask:0xf bank_mask:0xf
	global_load_dwordx4 v[40:43], v115, s[52:53]
	global_load_dwordx4 v[44:47], v116, s[52:53]
	s_lshl_b64 exec, s[22:23], 12
	v_mov_b32_e32 v85, v110
	v_mov_b32_e32 v89, s10
	s_mov_b64 exec, -1
.Lq_g12:
	s_add_u32 s11, s34, 48
	s_cmp_ge_u32 s11, s28
	s_cbranch_scc1 .Lq_end
	s_cmp_gt_u32 s50, 31
	s_cbranch_scc1 .Lq_stdg12
	s_add_u32 s36, s11, 20
	v_readlane_b32 s4, v81, s50
	s_cmp_lt_u32 s4, s36
	s_cbranch_scc1 .Lq_stxg12

; #define LAS __attribute__((address_space(3)))
; __device__ __forceinline__ int wave_isum4_t(const int (&d)[4], int lane) {
;     const bool o1 = lane & 1, o2 = lane & 2;
;     int a = o1 ? d[1] : d[0], b = o1 ? d[0] : d[1], c = o1 ? d[3] : d[2], e = o1 ? d[2] : d[3];
;     a += __builtin_amdgcn_update_dpp(0, b, 0xB1, 0xf, 0xf, true);
;     c += __builtin_amdgcn_update_dpp(0, e, 0xB1, 0xf, 0xf, true);
;     int f = o2 ? c : a, g = o2 ? a : c;
;     f += __builtin_amdgcn_update_dpp(0, g, 0x4E, 0xf, 0xf, true);
;     f += __builtin_amdgcn_update_dpp(0, f, 0x124, 0xf, 0xf, true);
;     f += __builtin_amdgcn_update_dpp(0, f, 0x128, 0xf, 0xf, true);
; __device__ __forceinline__ void peer3_dots(const u4 (&R)[PG][2], const u4 (&xq)[2], int sx15, LAS int* redrow, int g) {
;     ...
;     for (int k = 0; k < 4; ++k) { int a = 0, ah = 0;
; #pragma unroll
;         for (int q = 0; q < 4; ++q) { const unsigned w = R[k][0][q];
;             a = __builtin_amdgcn_sdot4((int)(w & 0x0f0f0f0fu), (int)xq[0][q], a, false); ah = __builtin_amdgcn_sdot4((int)(w & 0xf0f0f0f0u), (int)xq[1][q], ah, false); }
;         d[k] = 32 * a + 2 * ah - sx15; }
;     u4 w; w.x = (unsigned)d[0]; w.y = (unsigned)d[1]; w.z = (unsigned)d[2]; w.w = (unsigned)d[3];
;     *(LAS u4*)(redrow + 4 * g) = w;
.Lq_finret12:
	v_and_b32_e32 v95, 0xf0f0f0f, v0
	v_and_b32_e32 v99, 0xf0f0f0f0, v0
	v_and_b32_e32 v96, 0xf0f0f0f, v1
	v_and_b32_e32 v100, 0xf0f0f0f0, v1
	v_dot4_i32_i8 v103, v95, v64, 0
	v_dot4_i32_i8 v104, v99, v68, 0
	v_and_b32_e32 v97, 0xf0f0f0f, v2
	v_and_b32_e32 v101, 0xf0f0f0f0, v2
	v_dot4_i32_i8 v103, v96, v65, v103
	v_dot4_i32_i8 v104, v100, v69, v104
	v_and_b32_e32 v98, 0xf0f0f0f, v3
	v_and_b32_e32 v102, 0xf0f0f0f0, v3
	v_dot4_i32_i8 v103, v97, v66, v103
	v_dot4_i32_i8 v104, v101, v70, v104
	v_dot4_i32_i8 v103, v98, v67, v103
	v_dot4_i32_i8 v104, v102, v71, v104
	v_and_b32_e32 v95, 0xf0f0f0f, v4
	v_and_b32_e32 v99, 0xf0f0f0f0, v4
	v_and_b32_e32 v96, 0xf0f0f0f, v5
	v_and_b32_e32 v100, 0xf0f0f0f0, v5
	v_lshl_add_u32 v105, v103, 4, v104
	v_lshl_add_u32 v91, v105, 1, v72
	v_dot4_i32_i8 v126, v95, v64, 0
	v_dot4_i32_i8 v127, v99, v68, 0
	v_and_b32_e32 v97, 0xf0f0f0f, v6
	v_and_b32_e32 v101, 0xf0f0f0f0, v6
	v_dot4_i32_i8 v126, v96, v65, v126
	v_dot4_i32_i8 v127, v100, v69, v127
	v_and_b32_e32 v98, 0xf0f0f0f, v7
	v_and_b32_e32 v102, 0xf0f0f0f0, v7
	v_dot4_i32_i8 v126, v97, v66, v126
	v_dot4_i32_i8 v127, v101, v70, v127
	v_dot4_i32_i8 v126, v98, v67, v126
	v_dot4_i32_i8 v127, v102, v71, v127
	v_and_b32_e32 v95, 0xf0f0f0f, v8
	v_and_b32_e32 v99, 0xf0f0f0f0, v8
	v_and_b32_e32 v96, 0xf0f0f0f, v9
	v_and_b32_e32 v100, 0xf0f0f0f0, v9
	v_lshl_add_u32 v105, v126, 4, v127
	v_lshl_add_u32 v92, v105, 1, v72
	v_dot4_i32_i8 v103, v95, v64, 0
	v_dot4_i32_i8 v104, v99, v68, 0
	v_and_b32_e32 v97, 0xf0f0f0f, v10
	v_and_b32_e32 v101, 0xf0f0f0f0, v10
	v_dot4_i32_i8 v103, v96, v65, v103
	v_dot4_i32_i8 v104, v100, v69, v104
	v_and_b32_e32 v98, 0xf0f0f0f, v11
	v_and_b32_e32 v102, 0xf0f0f0f0, v11
	v_dot4_i32_i8 v103, v97, v66, v103
	v_dot4_i32_i8 v104, v101, v70, v104
	v_dot4_i32_i8 v103, v98, v67, v103
	v_dot4_i32_i8 v104, v102, v71, v104
	v_and_b32_e32 v95, 0xf0f0f0f, v12
	v_and_b32_e32 v99, 0xf0f0f0f0, v12
	v_and_b32_e32 v96, 0xf0f0f0f, v13
	v_and_b32_e32 v100, 0xf0f0f0f0, v13
	v_lshl_add_u32 v105, v103, 4, v104
	v_lshl_add_u32 v93, v105, 1, v72
	v_dot4_i32_i8 v126, v95, v64, 0
	v_dot4_i32_i8 v127, v99, v68, 0
	v_and_b32_e32 v97, 0xf0f0f0f, v14
	v_and_b32_e32 v101, 0xf0f0f0f0, v14
	v_dot4_i32_i8 v126, v96, v65, v126
	v_dot4_i32_i8 v127, v100, v69, v127
	v_and_b32_e32 v98, 0xf0f0f0f, v15
	v_and_b32_e32 v102, 0xf0f0f0f0, v15
	v_dot4_i32_i8 v126, v97, v66, v126
	v_dot4_i32_i8 v127, v101, v70, v127
	v_dot4_i32_i8 v126, v98, v67, v126
	v_dot4_i32_i8 v127, v102, v71, v127
	v_readlane_b32 s36, v75, 60
	v_readlane_b32 s5, v75, 61
	v_readlane_b32 s6, v75, 62
	v_lshl_add_u32 v105, v126, 4, v127
	v_lshl_add_u32 v94, v105, 1, v72
	v_cndmask_b32_e64 v107, v92, v91, s[38:39]
	v_cndmask_b32_e64 v109, v94, v93, s[38:39]
	v_cndmask_b32_e64 v106, v91, v92, s[38:39]
	v_cndmask_b32_e64 v108, v93, v94, s[38:39]
	v_add_u32_dpp v106, v107, v106 quad_perm:[1,0,3,2] row_mask:0xf bank_mask:0xf
	v_add_u32_dpp v108, v109, v108 quad_perm:[1,0,3,2] row_mask:0xf bank_mask:0xf
	v_readlane_b32 s7, v75, 63
	v_cndmask_b32_e64 v111, v108, v106, s[42:43]
	v_cndmask_b32_e64 v110, v106, v108, s[42:43]
	v_add_u32_e32 v113, s36, v206
	v_add_u32_e32 v114, s5, v206
	v_add_u32_dpp v110, v111, v110 quad_perm:[2,3,0,1] row_mask:0xf bank_mask:0xf
	v_add_u32_e32 v115, s6, v206
	v_add_u32_e32 v116, s7, v206
	v_add_u32_dpp v110, v110, v110 row_ror:4 row_mask:0xf bank_mask:0xf
	global_load_dwordx4 v[48:51], v113, s[52:53]
	global_load_dwordx4 v[52:55], v114, s[52:53]
	v_add_u32_dpp v110, v110, v110 row_ror:8 row_mask:0xf bank_mask:0xf
	global_load_dwordx4 v[56:59], v115, s[52:53]
	global_load_dwordx4 v[60:63], v116, s[52:53]
	s_mov_b64 exec, s[22:23]
	v_mov_b32_e32 v86, v110
	v_mov_b32_e32 v90, s10
	s_mov_b64 exec, -1
.Lq_g13:
	s_add_u32 s11, s34, 52
	s_cmp_ge_u32 s11, s28
	s_cbranch_scc1 .Lq_end
	s_cmp_gt_u32 s50, 31
	s_cbranch_scc1 .Lq_stdg13
	s_add_u32 s36, s11, 20
	v_readlane_b32 s4, v81, s50
	s_cmp_lt_u32 s4, s36
	s_cbranch_scc1 .Lq_stxg13

; #define LAS __attribute__((address_space(3)))
; __device__ __forceinline__ int wave_isum4_t(const int (&d)[4], int lane) {
;     const bool o1 = lane & 1, o2 = lane & 2;
;     int a = o1 ? d[1] : d[0], b = o1 ? d[0] : d[1], c = o1 ? d[3] : d[2], e = o1 ? d[2] : d[3];
;     a += __builtin_amdgcn_update_dpp(0, b, 0xB1, 0xf, 0xf, true);
;     c += __builtin_amdgcn_update_dpp(0, e, 0xB1, 0xf, 0xf, true);
;     int f = o2 ? c : a, g = o2 ? a : c;
;     f += __builtin_amdgcn_update_dpp(0, g, 0x4E, 0xf, 0xf, true);
;     f += __builtin_amdgcn_update_dpp(0, f, 0x124, 0xf, 0xf, true);
;     f += __builtin_amdgcn_update_dpp(0, f, 0x128, 0xf, 0xf, true);
; __device__ __forceinline__ void peer3_dots(const u4 (&R)[PG][2], const u4 (&xq)[2], int sx15, LAS int* redrow, int g) {
;     ...
;     for (int k = 0; k < 4; ++k) { int a = 0, ah = 0;
; #pragma unroll
;         for (int q = 0; q < 4; ++q) { const unsigned w = R[k][0][q];
;             a = __builtin_amdgcn_sdot4((int)(w & 0x0f0f0f0fu), (int)xq[0][q], a, false); ah = __builtin_amdgcn_sdot4((int)(w & 0xf0f0f0f0u), (int)xq[1][q], ah, false); }
;         d[k] = 32 * a + 2 * ah - sx15; }
;     u4 w; w.x = (unsigned)d[0]; w.y = (unsigned)d[1]; w.z = (unsigned)d[2]; w.w = (unsigned)d[3];
;     *(LAS u4*)(redrow + 4 * g) = w;
.Lq_finret13:
	v_and_b32_e32 v95, 0xf0f0f0f, v16
	v_and_b32_e32 v99, 0xf0f0f0f0, v16
	v_and_b32_e32 v96, 0xf0f0f0f, v17
	v_and_b32_e32 v100, 0xf0f0f0f0, v17
	v_dot4_i32_i8 v103, v95, v64, 0
	v_dot4_i32_i8 v104, v99, v68, 0
	v_and_b32_e32 v97, 0xf0f0f0f, v18
	v_and_b32_e32 v101, 0xf0f0f0f0, v18
	v_dot4_i32_i8 v103, v96, v65, v103
	v_dot4_i32_i8 v104, v100, v69, v104
	v_and_b32_e32 v98, 0xf0f0f0f, v19
	v_and_b32_e32 v102, 0xf0f0f0f0, v19
	v_dot4_i32_i8 v103, v97, v66, v103
	v_dot4_i32_i8 v104, v101, v70, v104
	v_dot4_i32_i8 v103, v98, v67, v103
	v_dot4_i32_i8 v104, v102, v71, v104
	v_and_b32_e32 v95, 0xf0f0f0f, v20
	v_and_b32_e32 v99, 0xf0f0f0f0, v20
	v_and_b32_e32 v96, 0xf0f0f0f, v21
	v_and_b32_e32 v100, 0xf0f0f0f0, v21
	v_lshl_add_u32 v105, v103, 4, v104
	v_lshl_add_u32 v91, v105, 1, v72
	v_dot4_i32_i8 v126, v95, v64, 0
	v_dot4_i32_i8 v127, v99, v68, 0
	v_and_b32_e32 v97, 0xf0f0f0f, v22
	v_and_b32_e32 v101, 0xf0f0f0f0, v22
	v_dot4_i32_i8 v126, v96, v65, v126
	v_dot4_i32_i8 v127, v100, v69, v127
	v_and_b32_e32 v98, 0xf0f0f0f, v23
	v_and_b32_e32 v102, 0xf0f0f0f0, v23
	v_dot4_i32_i8 v126, v97, v66, v126
	v_dot4_i32_i8 v127, v101, v70, v127
	v_dot4_i32_i8 v126, v98, v67, v126
	v_dot4_i32_i8 v127, v102, v71, v127
	v_and_b32_e32 v95, 0xf0f0f0f, v24
	v_and_b32_e32 v99, 0xf0f0f0f0, v24
	v_and_b32_e32 v96, 0xf0f0f0f, v25
	v_and_b32_e32 v100, 0xf0f0f0f0, v25
	v_lshl_add_u32 v105, v126, 4, v127
	v_lshl_add_u32 v92, v105, 1, v72
	v_dot4_i32_i8 v103, v95, v64, 0
	v_dot4_i32_i8 v104, v99, v68, 0
	v_and_b32_e32 v97, 0xf0f0f0f, v26
	v_and_b32_e32 v101, 0xf0f0f0f0, v26
	v_dot4_i32_i8 v103, v96, v65, v103
	v_dot4_i32_i8 v104, v100, v69, v104
	v_and_b32_e32 v98, 0xf0f0f0f, v27
	v_and_b32_e32 v102, 0xf0f0f0f0, v27
	v_dot4_i32_i8 v103, v97, v66, v103
	v_dot4_i32_i8 v104, v101, v70, v104
	v_dot4_i32_i8 v103, v98, v67, v103
	v_dot4_i32_i8 v104, v102, v71, v104
	v_and_b32_e32 v95, 0xf0f0f0f, v28
	v_and_b32_e32 v99, 0xf0f0f0f0, v28
	v_and_b32_e32 v96, 0xf0f0f0f, v29
	v_and_b32_e32 v100, 0xf0f0f0f0, v29
	v_lshl_add_u32 v105, v103, 4, v104
	v_lshl_add_u32 v93, v105, 1, v72
	v_dot4_i32_i8 v126, v95, v64, 0
	v_dot4_i32_i8 v127, v99, v68, 0
	v_and_b32_e32 v97, 0xf0f0f0f, v30
	v_and_b32_e32 v101, 0xf0f0f0f0, v30
	v_dot4_i32_i8 v126, v96, v65, v126
	v_dot4_i32_i8 v127, v100, v69, v127
	v_and_b32_e32 v98, 0xf0f0f0f, v31
	v_and_b32_e32 v102, 0xf0f0f0f0, v31
	v_dot4_i32_i8 v126, v97, v66, v126
	v_dot4_i32_i8 v127, v101, v70, v127
	v_dot4_i32_i8 v126, v98, v67, v126
	v_dot4_i32_i8 v127, v102, v71, v127
	v_lshlrev_b32_e32 v76, 10, v74
	s_nop 1
	v_readlane_b32 s36, v76, 0
	v_readlane_b32 s5, v76, 1
	v_readlane_b32 s6, v76, 2
	v_lshl_add_u32 v105, v126, 4, v127
	v_lshl_add_u32 v94, v105, 1, v72
	v_cndmask_b32_e64 v107, v92, v91, s[38:39]
	v_cndmask_b32_e64 v109, v94, v93, s[38:39]
	v_cndmask_b32_e64 v106, v91, v92, s[38:39]
	v_cndmask_b32_e64 v108, v93, v94, s[38:39]
	v_add_u32_dpp v106, v107, v106 quad_perm:[1,0,3,2] row_mask:0xf bank_mask:0xf
	v_add_u32_dpp v108, v109, v108 quad_perm:[1,0,3,2] row_mask:0xf bank_mask:0xf
	v_readlane_b32 s7, v76, 3
	v_cndmask_b32_e64 v111, v108, v106, s[42:43]
	v_cndmask_b32_e64 v110, v106, v108, s[42:43]
	v_add_u32_e32 v113, s36, v206
	v_add_u32_e32 v114, s5, v206
	v_add_u32_dpp v110, v111, v110 quad_perm:[2,3,0,1] row_mask:0xf bank_mask:0xf
	v_add_u32_e32 v115, s6, v206
	v_add_u32_e32 v116, s7, v206
	v_add_u32_dpp v110, v110, v110 row_ror:4 row_mask:0xf bank_mask:0xf
	global_load_dwordx4 v[0:3], v113, s[52:53]
	global_load_dwordx4 v[4:7], v114, s[52:53]
	v_add_u32_dpp v110, v110, v110 row_ror:8 row_mask:0xf bank_mask:0xf
	global_load_dwordx4 v[8:11], v115, s[52:53]
	global_load_dwordx4 v[12:15], v116, s[52:53]
	s_lshl_b64 exec, s[22:23], 4
	v_mov_b32_e32 v86, v110
	v_mov_b32_e32 v90, s10
	s_mov_b64 exec, -1
.Lq_g14:
	s_add_u32 s11, s34, 56
	s_cmp_ge_u32 s11, s28
	s_cbranch_scc1 .Lq_end
	s_cmp_gt_u32 s50, 31
	s_cbranch_scc1 .Lq_stdg14
	s_add_u32 s36, s11, 20
	v_readlane_b32 s4, v81, s50
	s_cmp_lt_u32 s4, s36
	s_cbranch_scc1 .Lq_stxg14

; #define LAS __attribute__((address_space(3)))
; __device__ __forceinline__ int wave_isum4_t(const int (&d)[4], int lane) {
;     const bool o1 = lane & 1, o2 = lane & 2;
;     int a = o1 ? d[1] : d[0], b = o1 ? d[0] : d[1], c = o1 ? d[3] : d[2], e = o1 ? d[2] : d[3];
;     a += __builtin_amdgcn_update_dpp(0, b, 0xB1, 0xf, 0xf, true);
;     c += __builtin_amdgcn_update_dpp(0, e, 0xB1, 0xf, 0xf, true);
;     int f = o2 ? c : a, g = o2 ? a : c;
;     f += __builtin_amdgcn_update_dpp(0, g, 0x4E, 0xf, 0xf, true);
;     f += __builtin_amdgcn_update_dpp(0, f, 0x124, 0xf, 0xf, true);
;     f += __builtin_amdgcn_update_dpp(0, f, 0x128, 0xf, 0xf, true);
; __device__ __forceinline__ void peer3_dots(const u4 (&R)[PG][2], const u4 (&xq)[2], int sx15, LAS int* redrow, int g) {
;     ...
;     for (int k = 0; k < 4; ++k) { int a = 0, ah = 0;
; #pragma unroll
;         for (int q = 0; q < 4; ++q) { const unsigned w = R[k][0][q];
;             a = __builtin_amdgcn_sdot4((int)(w & 0x0f0f0f0fu), (int)xq[0][q], a, false); ah = __builtin_amdgcn_sdot4((int)(w & 0xf0f0f0f0u), (int)xq[1][q], ah, false); }
;         d[k] = 32 * a + 2 * ah - sx15; }
;     u4 w; w.x = (unsigned)d[0]; w.y = (unsigned)d[1]; w.z = (unsigned)d[2]; w.w = (unsigned)d[3];
;     *(LAS u4*)(redrow + 4 * g) = w;
.Lq_finret14:
	v_and_b32_e32 v95, 0xf0f0f0f, v32
	v_and_b32_e32 v99, 0xf0f0f0f0, v32
	v_and_b32_e32 v96, 0xf0f0f0f, v33
	v_and_b32_e32 v100, 0xf0f0f0f0, v33
	v_dot4_i32_i8 v103, v95, v64, 0
	v_dot4_i32_i8 v104, v99, v68, 0
	v_and_b32_e32 v97, 0xf0f0f0f, v34
	v_and_b32_e32 v101, 0xf0f0f0f0, v34
	v_dot4_i32_i8 v103, v96, v65, v103
	v_dot4_i32_i8 v104, v100, v69, v104
	v_and_b32_e32 v98, 0xf0f0f0f, v35
	v_and_b32_e32 v102, 0xf0f0f0f0, v35
	v_dot4_i32_i8 v103, v97, v66, v103
	v_dot4_i32_i8 v104, v101, v70, v104
	v_dot4_i32_i8 v103, v98, v67, v103
	v_dot4_i32_i8 v104, v102, v71, v104
	v_and_b32_e32 v95, 0xf0f0f0f, v36
	v_and_b32_e32 v99, 0xf0f0f0f0, v36
	v_and_b32_e32 v96, 0xf0f0f0f, v37
	v_and_b32_e32 v100, 0xf0f0f0f0, v37
	v_lshl_add_u32 v105, v103, 4, v104
	v_lshl_add_u32 v91, v105, 1, v72
	v_dot4_i32_i8 v126, v95, v64, 0
	v_dot4_i32_i8 v127, v99, v68, 0
	v_and_b32_e32 v97, 0xf0f0f0f, v38
	v_and_b32_e32 v101, 0xf0f0f0f0, v38
	v_dot4_i32_i8 v126, v96, v65, v126
	v_dot4_i32_i8 v127, v100, v69, v127
	v_and_b32_e32 v98, 0xf0f0f0f, v39
	v_and_b32_e32 v102, 0xf0f0f0f0, v39
	v_dot4_i32_i8 v126, v97, v66, v126
	v_dot4_i32_i8 v127, v101, v70, v127
	v_dot4_i32_i8 v126, v98, v67, v126
	v_dot4_i32_i8 v127, v102, v71, v127
	v_and_b32_e32 v95, 0xf0f0f0f, v40
	v_and_b32_e32 v99, 0xf0f0f0f0, v40
	v_and_b32_e32 v96, 0xf0f0f0f, v41
	v_and_b32_e32 v100, 0xf0f0f0f0, v41
	v_lshl_add_u32 v105, v126, 4, v127
	v_lshl_add_u32 v92, v105, 1, v72
	v_dot4_i32_i8 v103, v95, v64, 0
	v_dot4_i32_i8 v104, v99, v68, 0
	v_and_b32_e32 v97, 0xf0f0f0f, v42
	v_and_b32_e32 v101, 0xf0f0f0f0, v42
	v_dot4_i32_i8 v103, v96, v65, v103
	v_dot4_i32_i8 v104, v100, v69, v104
	v_and_b32_e32 v98, 0xf0f0f0f, v43
	v_and_b32_e32 v102, 0xf0f0f0f0, v43
	v_dot4_i32_i8 v103, v97, v66, v103
	v_dot4_i32_i8 v104, v101, v70, v104
	v_dot4_i32_i8 v103, v98, v67, v103
	v_dot4_i32_i8 v104, v102, v71, v104
	v_and_b32_e32 v95, 0xf0f0f0f, v44
	v_and_b32_e32 v99, 0xf0f0f0f0, v44
	v_and_b32_e32 v96, 0xf0f0f0f, v45
	v_and_b32_e32 v100, 0xf0f0f0f0, v45
	v_lshl_add_u32 v105, v103, 4, v104
	v_lshl_add_u32 v93, v105, 1, v72
	v_dot4_i32_i8 v126, v95, v64, 0
	v_dot4_i32_i8 v127, v99, v68, 0
	v_and_b32_e32 v97, 0xf0f0f0f, v46
	v_and_b32_e32 v101, 0xf0f0f0f0, v46
	v_dot4_i32_i8 v126, v96, v65, v126
	v_dot4_i32_i8 v127, v100, v69, v127
	v_and_b32_e32 v98, 0xf0f0f0f, v47
	v_and_b32_e32 v102, 0xf0f0f0f0, v47
	v_dot4_i32_i8 v126, v97, v66, v126
	v_dot4_i32_i8 v127, v101, v70, v127
	v_dot4_i32_i8 v126, v98, v67, v126
	v_dot4_i32_i8 v127, v102, v71, v127
	v_readlane_b32 s36, v76, 4
	v_readlane_b32 s5, v76, 5
	v_readlane_b32 s6, v76, 6
	v_lshl_add_u32 v105, v126, 4, v127
	v_lshl_add_u32 v94, v105, 1, v72
	v_cndmask_b32_e64 v107, v92, v91, s[38:39]
	v_cndmask_b32_e64 v109, v94, v93, s[38:39]
	v_cndmask_b32_e64 v106, v91, v92, s[38:39]
	v_cndmask_b32_e64 v108, v93, v94, s[38:39]
	v_add_u32_dpp v106, v107, v106 quad_perm:[1,0,3,2] row_mask:0xf bank_mask:0xf
	v_add_u32_dpp v108, v109, v108 quad_perm:[1,0,3,2] row_mask:0xf bank_mask:0xf
	v_readlane_b32 s7, v76, 7
	v_cndmask_b32_e64 v111, v108, v106, s[42:43]
	v_cndmask_b32_e64 v110, v106, v108, s[42:43]
	v_add_u32_e32 v113, s36, v206
	v_add_u32_e32 v114, s5, v206
	v_add_u32_dpp v110, v111, v110 quad_perm:[2,3,0,1] row_mask:0xf bank_mask:0xf
	v_add_u32_e32 v115, s6, v206
	v_add_u32_e32 v116, s7, v206
	v_add_u32_dpp v110, v110, v110 row_ror:4 row_mask:0xf bank_mask:0xf
	global_load_dwordx4 v[16:19], v113, s[52:53]
	global_load_dwordx4 v[20:23], v114, s[52:53]
	v_add_u32_dpp v110, v110, v110 row_ror:8 row_mask:0xf bank_mask:0xf
	global_load_dwordx4 v[24:27], v115, s[52:53]
	global_load_dwordx4 v[28:31], v116, s[52:53]
	s_lshl_b64 exec, s[22:23], 8
	v_mov_b32_e32 v86, v110
	v_mov_b32_e32 v90, s10
	s_mov_b64 exec, -1
.Lq_g15:
	s_add_u32 s11, s34, 60
	s_cmp_ge_u32 s11, s28
	s_cbranch_scc1 .Lq_end
	s_cmp_gt_u32 s50, 31
	s_cbranch_scc1 .Lq_stdg15
	s_add_u32 s36, s11, 20
	v_readlane_b32 s4, v81, s50
	s_cmp_lt_u32 s4, s36
	s_cbranch_scc1 .Lq_stxg15

; #define LAS __attribute__((address_space(3)))
; __device__ __forceinline__ int wave_isum4_t(const int (&d)[4], int lane) {
;     const bool o1 = lane & 1, o2 = lane & 2;
;     int a = o1 ? d[1] : d[0], b = o1 ? d[0] : d[1], c = o1 ? d[3] : d[2], e = o1 ? d[2] : d[3];
;     a += __builtin_amdgcn_update_dpp(0, b, 0xB1, 0xf, 0xf, true);
;     c += __builtin_amdgcn_update_dpp(0, e, 0xB1, 0xf, 0xf, true);
;     int f = o2 ? c : a, g = o2 ? a : c;
;     f += __builtin_amdgcn_update_dpp(0, g, 0x4E, 0xf, 0xf, true);
;     f += __builtin_amdgcn_update_dpp(0, f, 0x124, 0xf, 0xf, true);
;     f += __builtin_amdgcn_update_dpp(0, f, 0x128, 0xf, 0xf, true);
; __device__ __forceinline__ void peer3_dots(const u4 (&R)[PG][2], const u4 (&xq)[2], int sx15, LAS int* redrow, int g) {
;     ...
;     for (int k = 0; k < 4; ++k) { int a = 0, ah = 0;
; #pragma unroll
;         for (int q = 0; q < 4; ++q) { const unsigned w = R[k][0][q];
;             a = __builtin_amdgcn_sdot4((int)(w & 0x0f0f0f0fu), (int)xq[0][q], a, false); ah = __builtin_amdgcn_sdot4((int)(w & 0xf0f0f0f0u), (int)xq[1][q], ah, false); }
;         d[k] = 32 * a + 2 * ah - sx15; }
;     u4 w; w.x = (unsigned)d[0]; w.y = (unsigned)d[1]; w.z = (unsigned)d[2]; w.w = (unsigned)d[3];
;     *(LAS u4*)(redrow + 4 * g) = w;
.Lq_finret15:
	v_and_b32_e32 v95, 0xf0f0f0f, v48
	v_and_b32_e32 v99, 0xf0f0f0f0, v48
	v_and_b32_e32 v96, 0xf0f0f0f, v49
	v_and_b32_e32 v100, 0xf0f0f0f0, v49
	v_dot4_i32_i8 v103, v95, v64, 0
	v_dot4_i32_i8 v104, v99, v68, 0
	v_and_b32_e32 v97, 0xf0f0f0f, v50
	v_and_b32_e32 v101, 0xf0f0f0f0, v50
	v_dot4_i32_i8 v103, v96, v65, v103
	v_dot4_i32_i8 v104, v100, v69, v104
	v_and_b32_e32 v98, 0xf0f0f0f, v51
	v_and_b32_e32 v102, 0xf0f0f0f0, v51
	v_dot4_i32_i8 v103, v97, v66, v103
	v_dot4_i32_i8 v104, v101, v70, v104
	v_dot4_i32_i8 v103, v98, v67, v103
	v_dot4_i32_i8 v104, v102, v71, v104
	v_and_b32_e32 v95, 0xf0f0f0f, v52
	v_and_b32_e32 v99, 0xf0f0f0f0, v52
	v_and_b32_e32 v96, 0xf0f0f0f, v53
	v_and_b32_e32 v100, 0xf0f0f0f0, v53
	v_lshl_add_u32 v105, v103, 4, v104
	v_lshl_add_u32 v91, v105, 1, v72
	v_dot4_i32_i8 v126, v95, v64, 0
	v_dot4_i32_i8 v127, v99, v68, 0
	v_and_b32_e32 v97, 0xf0f0f0f, v54
	v_and_b32_e32 v101, 0xf0f0f0f0, v54
	v_dot4_i32_i8 v126, v96, v65, v126
	v_dot4_i32_i8 v127, v100, v69, v127
	v_and_b32_e32 v98, 0xf0f0f0f, v55
	v_and_b32_e32 v102, 0xf0f0f0f0, v55
	v_dot4_i32_i8 v126, v97, v66, v126
	v_dot4_i32_i8 v127, v101, v70, v127
	v_dot4_i32_i8 v126, v98, v67, v126
	v_dot4_i32_i8 v127, v102, v71, v127
	v_and_b32_e32 v95, 0xf0f0f0f, v56
	v_and_b32_e32 v99, 0xf0f0f0f0, v56
	v_and_b32_e32 v96, 0xf0f0f0f, v57
	v_and_b32_e32 v100, 0xf0f0f0f0, v57
	v_lshl_add_u32 v105, v126, 4, v127
	v_lshl_add_u32 v92, v105, 1, v72
	v_dot4_i32_i8 v103, v95, v64, 0
	v_dot4_i32_i8 v104, v99, v68, 0
	v_and_b32_e32 v97, 0xf0f0f0f, v58
	v_and_b32_e32 v101, 0xf0f0f0f0, v58
	v_dot4_i32_i8 v103, v96, v65, v103
	v_dot4_i32_i8 v104, v100, v69, v104
	v_and_b32_e32 v98, 0xf0f0f0f, v59
	v_and_b32_e32 v102, 0xf0f0f0f0, v59
	v_dot4_i32_i8 v103, v97, v66, v103
	v_dot4_i32_i8 v104, v101, v70, v104
	v_dot4_i32_i8 v103, v98, v67, v103
	v_dot4_i32_i8 v104, v102, v71, v104
	v_and_b32_e32 v95, 0xf0f0f0f, v60
	v_and_b32_e32 v99, 0xf0f0f0f0, v60
	v_and_b32_e32 v96, 0xf0f0f0f, v61
	v_and_b32_e32 v100, 0xf0f0f0f0, v61
	v_lshl_add_u32 v105, v103, 4, v104
	v_lshl_add_u32 v93, v105, 1, v72
	v_dot4_i32_i8 v126, v95, v64, 0
	v_dot4_i32_i8 v127, v99, v68, 0
	v_and_b32_e32 v97, 0xf0f0f0f, v62
	v_and_b32_e32 v101, 0xf0f0f0f0, v62
	v_dot4_i32_i8 v126, v96, v65, v126
	v_dot4_i32_i8 v127, v100, v69, v127
	v_and_b32_e32 v98, 0xf0f0f0f, v63
	v_and_b32_e32 v102, 0xf0f0f0f0, v63
	v_dot4_i32_i8 v126, v97, v66, v126
	v_dot4_i32_i8 v127, v101, v70, v127
	v_dot4_i32_i8 v126, v98, v67, v126
	v_dot4_i32_i8 v127, v102, v71, v127
	v_readlane_b32 s36, v76, 8
	v_readlane_b32 s5, v76, 9
	v_readlane_b32 s6, v76, 10
	v_lshl_add_u32 v105, v126, 4, v127
	v_lshl_add_u32 v94, v105, 1, v72
	v_cndmask_b32_e64 v107, v92, v91, s[38:39]
	v_cndmask_b32_e64 v109, v94, v93, s[38:39]
	v_cndmask_b32_e64 v106, v91, v92, s[38:39]
	v_cndmask_b32_e64 v108, v93, v94, s[38:39]
	v_add_u32_dpp v106, v107, v106 quad_perm:[1,0,3,2] row_mask:0xf bank_mask:0xf
	v_add_u32_dpp v108, v109, v108 quad_perm:[1,0,3,2] row_mask:0xf bank_mask:0xf
	v_readlane_b32 s7, v76, 11
	v_cndmask_b32_e64 v111, v108, v106, s[42:43]
	v_cndmask_b32_e64 v110, v106, v108, s[42:43]
	v_add_u32_e32 v113, s36, v206
	v_add_u32_e32 v114, s5, v206
	v_add_u32_dpp v110, v111, v110 quad_perm:[2,3,0,1] row_mask:0xf bank_mask:0xf
	v_add_u32_e32 v115, s6, v206
	v_add_u32_e32 v116, s7, v206
	v_add_u32_dpp v110, v110, v110 row_ror:4 row_mask:0xf bank_mask:0xf
	global_load_dwordx4 v[32:35], v113, s[52:53]
	global_load_dwordx4 v[36:39], v114, s[52:53]
	v_add_u32_dpp v110, v110, v110 row_ror:8 row_mask:0xf bank_mask:0xf
	global_load_dwordx4 v[40:43], v115, s[52:53]
	global_load_dwordx4 v[44:47], v116, s[52:53]
	s_lshl_b64 exec, s[22:23], 12
	v_mov_b32_e32 v86, v110
	v_mov_b32_e32 v90, s10
	s_mov_b64 exec, -1
	s_branch .Lq_blockend

; __device__ __forceinline__ float gelu_tanh(float x) { return pg8::gelu_tanh_f(x); }
; __device__ __forceinline__ void phase_peer_bucket(const Params& P, unsigned char* ws, int l, LAS unsigned char* lds, int bid, int G, int lane, int wave) {
;     ...
;                 int dv = 0;
;                 int dv1 = 0, dv2 = 0, dv3 = 0;
; #pragma unroll
;                 for (int r_ = 0; r_ < 64; r_ += 4) { dv += red[r_ * 68 + lane]; dv1 += red[(r_ + 1) * 68 + lane]; dv2 += red[(r_ + 2) * 68 + lane]; dv3 += red[(r_ + 3) * 68 + lane]; }
;                 dv += dv1 + dv2 + dv3;
;                 if (lane < blen) { const float hwval = wv * gelu_tanh((float)dv * us * xsv) * vs; FHW[blk + lane] = hwval; hmax = fmaxf(hmax, fabsf(hwval)); }
.Lq_blockend:
	v_mov_b32_e32 v117, v83
	v_mov_b32_e32 v118, v84
	v_mov_b32_e32 v119, v85
	v_mov_b32_e32 v120, v86
	s_nop 1
	v_permlane16_swap_b32_e32 v83, v117
	v_permlane16_swap_b32_e32 v84, v118
	v_permlane16_swap_b32_e32 v85, v119
	v_permlane16_swap_b32_e32 v86, v120
	v_add_u32_e32 v83, v83, v117
	v_add_u32_e32 v84, v84, v118
	v_add_u32_e32 v85, v85, v119
	v_add_u32_e32 v86, v86, v120
	v_mov_b32_e32 v117, v83
	v_mov_b32_e32 v118, v84
	v_mov_b32_e32 v119, v85
	v_mov_b32_e32 v120, v86
	s_nop 1
	v_permlane32_swap_b32_e32 v83, v117
	v_permlane32_swap_b32_e32 v84, v118
	v_permlane32_swap_b32_e32 v85, v119
	v_permlane32_swap_b32_e32 v86, v120
	v_add_u32_e32 v83, v83, v117
	v_add_u32_e32 v84, v84, v118
	v_add_u32_e32 v85, v85, v119
	v_add_u32_e32 v86, v86, v120
	v_lshrrev_b32_e32 v124, 4, v208
	v_cmp_eq_u32_e64 s[4:5], 1, v124
	v_cmp_eq_u32_e64 s[6:7], 2, v124
	v_cmp_eq_u32_e32 vcc, 3, v124
	s_nop 1
	v_cndmask_b32_e64 v121, v83, v84, s[4:5]
	v_cndmask_b32_e64 v122, v87, v88, s[4:5]
	v_cndmask_b32_e64 v121, v121, v85, s[6:7]
	v_cndmask_b32_e64 v122, v122, v89, s[6:7]
	v_cndmask_b32_e32 v121, v121, v86, vcc
	v_cndmask_b32_e32 v122, v122, v90, vcc
	v_cvt_f32_i32_e32 v121, v121
	v_mul_f32_e32 v121, v79, v121
	v_mul_f32_e32 v121, v122, v121
	v_mul_f32_e32 v123, 0x3d372713, v121
	v_mul_f32_e32 v123, v121, v123
	v_fma_f32 v123, v121, v123, v121
	v_mul_f32_e32 v123, 0xbfcc422a, v123
	v_mul_f32_e32 v123, 0x3fb8aa3b, v123
	v_exp_f32_e32 v123, v123
	s_nop 0
	v_add_f32_e32 v123, 1.0, v123
	v_rcp_f32_e32 v123, v123
	s_nop 0
	v_mul_f32_e32 v121, v121, v123
	v_mul_f32_e32 v121, v77, v121
	v_mul_f32_e32 v123, v82, v121
	v_add_u32_e32 v124, s34, v208
	v_cmp_gt_u32_e32 vcc, s28, v124
	v_lshlrev_b32_e32 v124, 2, v124
	s_and_saveexec_b64 s[6:7], vcc
	global_store_dword v124, v123, s[16:17]
	v_max_f32_e32 v121, v233, v233
	v_max_f32_e64 v233, v121, |v123|
	s_or_b64 exec, exec, s[6:7]
	s_add_u32 s34, s34, 64
	s_cmp_lt_u32 s34, s28
	s_cbranch_scc1 .Lq_block
	s_waitcnt vmcnt(0)
	s_mov_b32 s36, 0
	s_branch .LBB0_1276
.Lq_sw0:
	s_mov_b32 s30, s31
	s_add_u32 s4, s30, 1
	v_readlane_b32 s35, v81, s4
	s_add_u32 s31, s30, 1

; #define PU_SX() do { int a_ = 0, b_ = 0; _Pragma("unroll") for (int q_ = 0; q_ < 4; ++q_) { a_ = __builtin_amdgcn_sdot4((int)xq[0][q_], 0x01010101, a_, false); b_ = __builtin_amdgcn_sdot4((int)xq[1][q_], 0x01010101, b_, false); } sx15 = 240 * a_ - 16 * b_; } while (0)
; __device__ __forceinline__ void phase_peer_bucket(const Params& P, unsigned char* ws, int l, LAS unsigned char* lds, int bid, int G, int lane, int wave) {
;     ...
;             int sx15; PU_SX();
.Lq_nnd10:
	s_and_b32 s4, s9, 7
	s_mul_i32 s4, s4, 0x810
	s_add_u32 s4, s100, s4
	s_add_u32 s9, s9, 1
	v_add_u32_e32 v117, s4, v206
	v_readlane_b32 s10, v201, s30
	ds_read_b128 v[64:67], v117
	ds_read_b128 v[68:71], v117 offset:1024
	s_waitcnt lgkmcnt(0)
	v_dot4_i32_i8 v118, v64, s65, 0
	v_dot4_i32_i8 v119, v68, s65, 0
	v_dot4_i32_i8 v118, v65, s65, v118
	v_dot4_i32_i8 v119, v69, s65, v119
	v_dot4_i32_i8 v118, v66, s65, v118
	v_dot4_i32_i8 v119, v70, s65, v119
	v_dot4_i32_i8 v118, v67, s65, v118
	v_dot4_i32_i8 v119, v71, s65, v119
	s_nop 2
	v_mul_i32_i24_e32 v118, 0xf0, v118
	v_lshlrev_b32_e32 v119, 4, v119
	v_sub_u32_e32 v72, v119, v118
	s_branch .Lq_swret0

; __device__ __forceinline__ int peer3_next_nonempty(int gstv, int t) {
;     while (t < 32 && __builtin_amdgcn_readlane(gstv, t + 1) == __builtin_amdgcn_readlane(gstv, t)) ++t;
;     return t;
; }
.Lq_stxg0:
	s_and_b32 s4, s56, 7
	s_mul_i32 s4, s4, 0x810
	s_add_u32 s44, s100, s4
	s_lshl_b32 s5, s50, 11
	s_add_u32 s6, s26, s5
	s_addc_u32 s7, s27, 0
	s_add_u32 s56, s56, 1
	global_load_dwordx4 v[128:131], v206, s[6:7] nt
	global_load_dwordx4 v[132:135], v206, s[6:7] offset:1024 nt
	s_bitset1_b32 s62, 0
	s_add_u32 s50, s50, 1
.Lq_nn26:
	s_cmp_gt_u32 s50, 31
	s_cbranch_scc1 .Lq_nnd26
	s_add_u32 s4, s50, 1
	v_readlane_b32 s5, v81, s4
	v_readlane_b32 s6, v81, s50
	s_cmp_lg_u32 s5, s6
	s_cbranch_scc1 .Lq_nnd26
	s_add_u32 s50, s50, 1
	s_branch .Lq_nn26
.Lq_nnd26:
	s_branch .Lq_stdg0
.Lq_stxg1:
	s_and_b32 s4, s56, 7
	s_mul_i32 s4, s4, 0x810
	s_add_u32 s45, s100, s4
	s_lshl_b32 s5, s50, 11
	s_add_u32 s6, s26, s5
	s_addc_u32 s7, s27, 0
	s_add_u32 s56, s56, 1
	global_load_dwordx4 v[136:139], v206, s[6:7] nt
	global_load_dwordx4 v[140:143], v206, s[6:7] offset:1024 nt
	s_bitset1_b32 s62, 1
	s_add_u32 s50, s50, 1
.Lq_nn27:
	s_cmp_gt_u32 s50, 31
	s_cbranch_scc1 .Lq_nnd27
	s_add_u32 s4, s50, 1
	v_readlane_b32 s5, v81, s4
	v_readlane_b32 s6, v81, s50
	s_cmp_lg_u32 s5, s6
	s_cbranch_scc1 .Lq_nnd27
	s_add_u32 s50, s50, 1
	s_branch .Lq_nn27
.Lq_nnd27:
	s_branch .Lq_stdg1
.Lq_stxg2:
	s_and_b32 s4, s56, 7
	s_mul_i32 s4, s4, 0x810
	s_add_u32 s46, s100, s4
	s_lshl_b32 s5, s50, 11
	s_add_u32 s6, s26, s5
	s_addc_u32 s7, s27, 0
	s_add_u32 s56, s56, 1
	global_load_dwordx4 v[144:147], v206, s[6:7] nt
	global_load_dwordx4 v[148:151], v206, s[6:7] offset:1024 nt
	s_bitset1_b32 s62, 2
	s_add_u32 s50, s50, 1
.Lq_nn28:
	s_cmp_gt_u32 s50, 31
	s_cbranch_scc1 .Lq_nnd28
	s_add_u32 s4, s50, 1
	v_readlane_b32 s5, v81, s4
	v_readlane_b32 s6, v81, s50
	s_cmp_lg_u32 s5, s6
	s_cbranch_scc1 .Lq_nnd28
	s_add_u32 s50, s50, 1
	s_branch .Lq_nn28
.Lq_nnd28:
	s_branch .Lq_stdg2
.Lq_stxg3:
	s_and_b32 s4, s56, 7
	s_mul_i32 s4, s4, 0x810
	s_add_u32 s47, s100, s4
	s_lshl_b32 s5, s50, 11
	s_add_u32 s6, s26, s5
	s_addc_u32 s7, s27, 0
	s_add_u32 s56, s56, 1
	global_load_dwordx4 v[152:155], v206, s[6:7] nt
	global_load_dwordx4 v[156:159], v206, s[6:7] offset:1024 nt
	s_bitset1_b32 s62, 3
	s_add_u32 s50, s50, 1
.Lq_nn29:
	s_cmp_gt_u32 s50, 31
	s_cbranch_scc1 .Lq_nnd29
	s_add_u32 s4, s50, 1
	v_readlane_b32 s5, v81, s4
	v_readlane_b32 s6, v81, s50
	s_cmp_lg_u32 s5, s6
	s_cbranch_scc1 .Lq_nnd29
	s_add_u32 s50, s50, 1
	s_branch .Lq_nn29
.Lq_nnd29:
	s_branch .Lq_stdg3

; __device__ __forceinline__ int peer3_next_nonempty(int gstv, int t) {
;     while (t < 32 && __builtin_amdgcn_readlane(gstv, t + 1) == __builtin_amdgcn_readlane(gstv, t)) ++t;
;     return t;
; }
.Lq_nn30:
	s_cmp_gt_u32 s50, 31
	s_cbranch_scc1 .Lq_nnd30
	s_add_u32 s4, s50, 1
	v_readlane_b32 s5, v81, s4
	v_readlane_b32 s6, v81, s50
	s_cmp_lg_u32 s5, s6
	s_cbranch_scc1 .Lq_nnd30
	s_add_u32 s50, s50, 1
	s_branch .Lq_nn30
.Lq_nnd30:
	s_branch .Lq_stdg4

; __device__ __forceinline__ int peer3_next_nonempty(int gstv, int t) {
;     while (t < 32 && __builtin_amdgcn_readlane(gstv, t + 1) == __builtin_amdgcn_readlane(gstv, t)) ++t;
;     return t;
; }
.Lq_nn31:
	s_cmp_gt_u32 s50, 31
	s_cbranch_scc1 .Lq_nnd31
	s_add_u32 s4, s50, 1
	v_readlane_b32 s5, v81, s4
	v_readlane_b32 s6, v81, s50
	s_cmp_lg_u32 s5, s6
	s_cbranch_scc1 .Lq_nnd31
	s_add_u32 s50, s50, 1
	s_branch .Lq_nn31
.Lq_nnd31:
	s_branch .Lq_stdg5

; __device__ __forceinline__ int peer3_next_nonempty(int gstv, int t) {
;     while (t < 32 && __builtin_amdgcn_readlane(gstv, t + 1) == __builtin_amdgcn_readlane(gstv, t)) ++t;
;     return t;
; }
.Lq_nn32:
	s_cmp_gt_u32 s50, 31
	s_cbranch_scc1 .Lq_nnd32
	s_add_u32 s4, s50, 1
	v_readlane_b32 s5, v81, s4
	v_readlane_b32 s6, v81, s50
	s_cmp_lg_u32 s5, s6
	s_cbranch_scc1 .Lq_nnd32
	s_add_u32 s50, s50, 1
	s_branch .Lq_nn32
.Lq_nnd32:
	s_branch .Lq_stdg6

; __device__ __forceinline__ int peer3_next_nonempty(int gstv, int t) {
;     while (t < 32 && __builtin_amdgcn_readlane(gstv, t + 1) == __builtin_amdgcn_readlane(gstv, t)) ++t;
;     return t;
; }
.Lq_nn33:
	s_cmp_gt_u32 s50, 31
	s_cbranch_scc1 .Lq_nnd33
	s_add_u32 s4, s50, 1
	v_readlane_b32 s5, v81, s4
	v_readlane_b32 s6, v81, s50
	s_cmp_lg_u32 s5, s6
	s_cbranch_scc1 .Lq_nnd33
	s_add_u32 s50, s50, 1
	s_branch .Lq_nn33
.Lq_nnd33:
	s_branch .Lq_stdg7

; __device__ __forceinline__ int peer3_next_nonempty(int gstv, int t) {
;     while (t < 32 && __builtin_amdgcn_readlane(gstv, t + 1) == __builtin_amdgcn_readlane(gstv, t)) ++t;
;     return t;
; }
.Lq_nn34:
	s_cmp_gt_u32 s50, 31
	s_cbranch_scc1 .Lq_nnd34
	s_add_u32 s4, s50, 1
	v_readlane_b32 s5, v81, s4
	v_readlane_b32 s6, v81, s50
	s_cmp_lg_u32 s5, s6
	s_cbranch_scc1 .Lq_nnd34
	s_add_u32 s50, s50, 1
	s_branch .Lq_nn34
.Lq_nnd34:
	s_branch .Lq_stdg8

; __device__ __forceinline__ int peer3_next_nonempty(int gstv, int t) {
;     while (t < 32 && __builtin_amdgcn_readlane(gstv, t + 1) == __builtin_amdgcn_readlane(gstv, t)) ++t;
;     return t;
; }
.Lq_nn35:
	s_cmp_gt_u32 s50, 31
	s_cbranch_scc1 .Lq_nnd35
	s_add_u32 s4, s50, 1
	v_readlane_b32 s5, v81, s4
	v_readlane_b32 s6, v81, s50
	s_cmp_lg_u32 s5, s6
	s_cbranch_scc1 .Lq_nnd35
	s_add_u32 s50, s50, 1
	s_branch .Lq_nn35
.Lq_nnd35:
	s_branch .Lq_stdg9

; __device__ __forceinline__ int peer3_next_nonempty(int gstv, int t) {
;     while (t < 32 && __builtin_amdgcn_readlane(gstv, t + 1) == __builtin_amdgcn_readlane(gstv, t)) ++t;
;     return t;
; }
.Lq_nn36:
	s_cmp_gt_u32 s50, 31
	s_cbranch_scc1 .Lq_nnd36
	s_add_u32 s4, s50, 1
	v_readlane_b32 s5, v81, s4
	v_readlane_b32 s6, v81, s50
	s_cmp_lg_u32 s5, s6
	s_cbranch_scc1 .Lq_nnd36
	s_add_u32 s50, s50, 1
	s_branch .Lq_nn36
.Lq_nnd36:
	s_branch .Lq_stdg10

; __device__ __forceinline__ int peer3_next_nonempty(int gstv, int t) {
;     while (t < 32 && __builtin_amdgcn_readlane(gstv, t + 1) == __builtin_amdgcn_readlane(gstv, t)) ++t;
;     return t;
; }
.Lq_nn37:
	s_cmp_gt_u32 s50, 31
	s_cbranch_scc1 .Lq_nnd37
	s_add_u32 s4, s50, 1
	v_readlane_b32 s5, v81, s4
	v_readlane_b32 s6, v81, s50
	s_cmp_lg_u32 s5, s6
	s_cbranch_scc1 .Lq_nnd37
	s_add_u32 s50, s50, 1
	s_branch .Lq_nn37
.Lq_nnd37:
	s_branch .Lq_stdg11

; __device__ __forceinline__ int peer3_next_nonempty(int gstv, int t) {
;     while (t < 32 && __builtin_amdgcn_readlane(gstv, t + 1) == __builtin_amdgcn_readlane(gstv, t)) ++t;
;     return t;
; }
.Lq_nn38:
	s_cmp_gt_u32 s50, 31
	s_cbranch_scc1 .Lq_nnd38
	s_add_u32 s4, s50, 1
	v_readlane_b32 s5, v81, s4
	v_readlane_b32 s6, v81, s50
	s_cmp_lg_u32 s5, s6
	s_cbranch_scc1 .Lq_nnd38
	s_add_u32 s50, s50, 1
	s_branch .Lq_nn38
.Lq_nnd38:
	s_branch .Lq_stdg12

; __device__ __forceinline__ int peer3_next_nonempty(int gstv, int t) {
;     while (t < 32 && __builtin_amdgcn_readlane(gstv, t + 1) == __builtin_amdgcn_readlane(gstv, t)) ++t;
;     return t;
; }
.Lq_nn39:
	s_cmp_gt_u32 s50, 31
	s_cbranch_scc1 .Lq_nnd39
	s_add_u32 s4, s50, 1
	v_readlane_b32 s5, v81, s4
	v_readlane_b32 s6, v81, s50
	s_cmp_lg_u32 s5, s6
	s_cbranch_scc1 .Lq_nnd39
	s_add_u32 s50, s50, 1
	s_branch .Lq_nn39
.Lq_nnd39:
	s_branch .Lq_stdg13

; __device__ __forceinline__ int peer3_next_nonempty(int gstv, int t) {
;     while (t < 32 && __builtin_amdgcn_readlane(gstv, t + 1) == __builtin_amdgcn_readlane(gstv, t)) ++t;
;     return t;
; }
.Lq_nn40:
	s_cmp_gt_u32 s50, 31
	s_cbranch_scc1 .Lq_nnd40
	s_add_u32 s4, s50, 1
	v_readlane_b32 s5, v81, s4
	v_readlane_b32 s6, v81, s50
	s_cmp_lg_u32 s5, s6
	s_cbranch_scc1 .Lq_nnd40
	s_add_u32 s50, s50, 1
	s_branch .Lq_nn40
.Lq_nnd40:
	s_branch .Lq_stdg14

; __device__ __forceinline__ int peer3_next_nonempty(int gstv, int t) {
;     while (t < 32 && __builtin_amdgcn_readlane(gstv, t + 1) == __builtin_amdgcn_readlane(gstv, t)) ++t;
;     return t;
; }
.Lq_nn41:
	s_cmp_gt_u32 s50, 31
	s_cbranch_scc1 .Lq_nnd41
	s_add_u32 s4, s50, 1
	v_readlane_b32 s5, v81, s4
	v_readlane_b32 s6, v81, s50
	s_cmp_lg_u32 s5, s6
	s_cbranch_scc1 .Lq_nnd41
	s_add_u32 s50, s50, 1
	s_branch .Lq_nn41
.Lq_nnd41:
	s_branch .Lq_stdg15
.Lq_fin0:
	v_add_u32_e32 v117, s45, v206
	s_bitset0_b32 s62, 1
	ds_write_b128 v117, v[136:139]
	ds_write_b128 v117, v[140:143] offset:1024
	s_branch .Lq_finret0
.Lq_fin1:
	v_add_u32_e32 v117, s46, v206
	s_bitset0_b32 s62, 2
	ds_write_b128 v117, v[144:147]
	ds_write_b128 v117, v[148:151] offset:1024
	s_branch .Lq_finret1
.Lq_fin2:
	v_add_u32_e32 v117, s47, v206
	s_bitset0_b32 s62, 3
	ds_write_b128 v117, v[152:155]
	ds_write_b128 v117, v[156:159] offset:1024
	s_branch .Lq_finret2
.Lq_fin3:
	v_add_u32_e32 v117, s44, v206
	s_bitset0_b32 s62, 0
	ds_write_b128 v117, v[128:131]
	ds_write_b128 v117, v[132:135] offset:1024
	s_branch .Lq_finret3

; __global__ void __launch_bounds__(512, 2) mk_fwd(Params P) {
	.amdhsa_kernel _Z6mk_fwd6Params
		.amdhsa_group_segment_fixed_size 0
		.amdhsa_private_segment_fixed_size 0
		.amdhsa_kernarg_size 760
		.amdhsa_user_sgpr_count 2
		.amdhsa_user_sgpr_dispatch_ptr 0
		.amdhsa_user_sgpr_queue_ptr 0
		.amdhsa_user_sgpr_kernarg_segment_ptr 1
		.amdhsa_user_sgpr_dispatch_id 0
		.amdhsa_user_sgpr_kernarg_preload_length 0
		.amdhsa_user_sgpr_kernarg_preload_offset 0
		.amdhsa_user_sgpr_private_segment_size 0
		.amdhsa_uses_dynamic_stack 0
		.amdhsa_enable_private_segment 0
		.amdhsa_system_sgpr_workgroup_id_x 1
		.amdhsa_system_sgpr_workgroup_id_y 0
		.amdhsa_system_sgpr_workgroup_id_z 0
		.amdhsa_system_sgpr_workgroup_info 0
		.amdhsa_system_vgpr_workitem_id 0
		.amdhsa_next_free_vgpr 256
		.amdhsa_next_free_sgpr 102
		.amdhsa_accum_offset 256
		.amdhsa_reserve_vcc 1
		.amdhsa_float_round_mode_32 0
		.amdhsa_float_round_mode_16_64 0
		.amdhsa_float_denorm_mode_32 3
		.amdhsa_float_denorm_mode_16_64 3
		.amdhsa_dx10_clamp 1
		.amdhsa_ieee_mode 1
		.amdhsa_fp16_overflow 0
		.amdhsa_tg_split 0
		.amdhsa_exception_fp_ieee_invalid_op 0
		.amdhsa_exception_fp_denorm_src 0
		.amdhsa_exception_fp_ieee_div_zero 0
		.amdhsa_exception_fp_ieee_overflow 0
		.amdhsa_exception_fp_ieee_underflow 0
		.amdhsa_exception_fp_ieee_inexact 0
		.amdhsa_exception_int_div_zero 0
	.end_amdhsa_kernel

; __global__ void __launch_bounds__(512, 2) mk_fwd(Params P) {
amdhsa.kernels:
  - .agpr_count:     0
    .args:
      - .offset:         0
        .size:           504
        .value_kind:     by_value
      - .offset:         504
        .size:           4
        .value_kind:     hidden_block_count_x
      - .offset:         508
        .size:           4
        .value_kind:     hidden_block_count_y
      - .offset:         512
        .size:           4
        .value_kind:     hidden_block_count_z
      - .offset:         516
        .size:           2
        .value_kind:     hidden_group_size_x
      - .offset:         518
        .size:           2
        .value_kind:     hidden_group_size_y
      - .offset:         520
        .size:           2
        .value_kind:     hidden_group_size_z
      - .offset:         522
        .size:           2
        .value_kind:     hidden_remainder_x
      - .offset:         524
        .size:           2
        .value_kind:     hidden_remainder_y
      - .offset:         526
        .size:           2
        .value_kind:     hidden_remainder_z
      - .offset:         544
        .size:           8
        .value_kind:     hidden_global_offset_x
      - .offset:         552
        .size:           8
        .value_kind:     hidden_global_offset_y
      - .offset:         560
        .size:           8
        .value_kind:     hidden_global_offset_z
      - .offset:         568
        .size:           2
        .value_kind:     hidden_grid_dims
      - .offset:         624
        .size:           4
        .value_kind:     hidden_dynamic_lds_size
    .group_segment_fixed_size: 0
    .kernarg_segment_align: 8
    .kernarg_segment_size: 760
    .language:       OpenCL C
    .language_version:
      - 2
      - 0
    .max_flat_workgroup_size: 512
    .name:           _Z6mk_fwd6Params
    .private_segment_fixed_size: 0
    .sgpr_count:     108
    .sgpr_spill_count: 203
    .symbol:         _Z6mk_fwd6Params.kd
    .uniform_work_group_size: 1
    .uses_dynamic_stack: false
    .vgpr_count:     256
    .vgpr_spill_count: 0
    .wavefront_size: 64
